# softmax row sums on the matrix pipe (ones x packed P MFMA), memory K/V projection GEMM moved from the tail of phase 2 (4 busy workgroups) in front of the MLA loop with those workgroups exempt from bac
# speedup vs baseline: 1.0595x; 1.0278x over previous
_Z10hybrid_fwd6Params:
	s_mov_b32 s32, 0
	s_load_dwordx4 s[4:7], s[0:1], 0x160
	s_mov_b32 s62, s2
	s_load_dwordx2 s[2:3], s[0:1], 0x290
	v_readfirstlane_b32 s28, v0
	s_waitcnt lgkmcnt(0)
	v_writelane_b32 v236, s4, 0
	s_nop 1
	v_writelane_b32 v236, s5, 1
	v_writelane_b32 v236, s6, 2
	v_writelane_b32 v236, s7, 3
	s_load_dwordx8 s[4:11], s[0:1], 0x140
	s_waitcnt lgkmcnt(0)
	v_writelane_b32 v236, s4, 4
	s_nop 1
	v_writelane_b32 v236, s5, 5
	v_writelane_b32 v236, s6, 6
	v_writelane_b32 v236, s7, 7
	v_writelane_b32 v236, s8, 8
	v_writelane_b32 v236, s9, 9
	v_writelane_b32 v236, s10, 10
	v_writelane_b32 v236, s11, 11
	s_load_dwordx4 s[4:7], s[0:1], 0x280
	v_writelane_b32 v236, s2, 12
	s_nop 1
	v_writelane_b32 v236, s3, 13
	s_waitcnt lgkmcnt(0)
	v_writelane_b32 v236, s4, 14
	s_load_dwordx8 s[84:91], s[0:1], 0x260
	s_load_dwordx2 s[2:3], s[0:1], 0x2d0
	v_writelane_b32 v236, s5, 15
	v_writelane_b32 v236, s6, 16
	v_writelane_b32 v236, s7, 17
	s_load_dwordx4 s[4:7], s[0:1], 0x2c0
	s_waitcnt lgkmcnt(0)
	v_writelane_b32 v236, s2, 18
	s_nop 1
	v_writelane_b32 v236, s3, 19
	v_writelane_b32 v236, s4, 20
	s_add_u32 s2, s0, 0x338
	s_addc_u32 s3, s1, 0
	v_writelane_b32 v236, s5, 21
	v_writelane_b32 v236, s6, 22
	v_writelane_b32 v236, s7, 23
	s_load_dwordx2 s[94:95], s[0:1], 0x330
	s_load_dword s82, s[0:1], 0x338
	s_load_dwordx8 s[4:11], s[0:1], 0x2a0
	s_waitcnt lgkmcnt(0)
	v_writelane_b32 v236, s4, 24
	s_nop 1
	v_writelane_b32 v236, s5, 25
	v_writelane_b32 v236, s6, 26
	v_writelane_b32 v236, s7, 27
	v_writelane_b32 v236, s8, 28
	v_writelane_b32 v236, s9, 29
	v_writelane_b32 v236, s10, 30
	v_writelane_b32 v236, s11, 31
	v_writelane_b32 v236, s2, 32
	s_nop 1
	v_writelane_b32 v236, s3, 33
	s_and_b32 s3, s82, 7
	s_mov_b32 s2, 0
	s_cmp_lg_u32 s3, 0
	v_writelane_b32 v236, s62, 34
	s_cbranch_scc1 .LBB0_2
	v_readlane_b32 s6, v236, 34
	s_ashr_i32 s4, s6, 31
	s_lshr_b32 s4, s4, 29
	s_add_i32 s4, s6, s4
	s_and_b32 s5, s4, -8
	s_ashr_i32 s3, s82, 3
	s_sub_i32 s5, s6, s5
	s_mul_i32 s3, s3, s5
	s_ashr_i32 s4, s4, 3
	s_add_i32 s62, s3, s4

.LBB0_920:
	s_mov_b32 s32, 0
	v_readfirstlane_b32 s4, v0
	s_branch .LBB0_936

.LBB0_936:
	s_cmp_eq_u32 s32, 1
	s_cbranch_scc1 .Lmemkv_ret
	s_cmp_gt_i32 s95, 3
	s_cselect_b64 s[0:1], -1, 0
	s_and_b64 s[2:3], s[80:81], s[0:1]
	v_readlane_b32 s52, v237, 21
	s_andn2_b64 vcc, exec, s[2:3]
	v_readlane_b32 s56, v237, 25
	v_readlane_b32 s57, v237, 26
	v_readlane_b32 s53, v237, 22
	v_readlane_b32 s54, v237, 23
	v_readlane_b32 s55, v237, 24
	v_readlane_b32 s58, v237, 27
	v_readlane_b32 s59, v237, 28
	s_cbranch_vccnz .LBB0_986
	s_waitcnt vmcnt(0)
	v_cmp_eq_u32_e32 vcc, 0, v0
	s_waitcnt vmcnt(0)
	s_barrier
	s_and_saveexec_b64 s[2:3], vcc
	s_cbranch_execz .LBB0_985
	v_readlane_b32 s4, v238, 32
	s_waitcnt vmcnt(0) expcnt(0) lgkmcnt(0)
	s_nop 0
	v_mov_b32_e32 v1, s4
	ds_read_b32 v3, v1
	ds_read_b32 v2, v1 offset:4
	s_waitcnt lgkmcnt(1)
	v_cmp_ne_u32_e32 vcc, 0, v3
	s_cbranch_vccnz .LBB0_953
	v_readlane_b32 s4, v236, 32
	v_readlane_b32 s5, v236, 33
	v_readlane_b32 s36, v237, 29
	s_load_dwordx2 s[8:9], s[4:5], 0x4
	v_readlane_b32 s48, v237, 41
	v_readlane_b32 s49, v237, 42
	s_add_u32 s4, s48, 0x4200
	s_addc_u32 s5, s49, 0
	s_add_u32 s6, s48, 0x4400
	s_addc_u32 s7, s49, 0
	s_waitcnt lgkmcnt(0)
	s_mul_i32 s33, s8, s82
	s_add_u32 s8, s48, 0x4500
	s_mul_i32 s33, s33, s9
	s_addc_u32 s9, s49, 0
	s_add_u32 s10, s48, 0x4600
	s_addc_u32 s11, s49, 0
	s_add_u32 s12, s48, 0x4700
	s_addc_u32 s13, s49, 0
	s_add_u32 s14, s48, 0x4800
	s_addc_u32 s15, s49, 0
	s_add_u32 s24, s48, 0x4900
	s_addc_u32 s25, s49, 0
	s_add_u32 s26, s48, 0x4a00
	s_addc_u32 s27, s49, 0
	s_add_u32 s28, s48, 0x4b00
	s_addc_u32 s29, s49, 0
	s_add_u32 s30, s48, 0x4c00
	s_addc_u32 s31, s49, 0
	s_add_u32 s34, s48, 0x4d00
	s_addc_u32 s35, s49, 0
	v_readlane_b32 s37, v237, 30
	s_add_u32 s36, s48, 0x4e00
	v_readlane_b32 s38, v237, 31
	s_addc_u32 s37, s49, 0
	v_readlane_b32 s39, v237, 32
	s_add_u32 s38, s48, 0x4f00
	v_readlane_b32 s40, v237, 33
	s_addc_u32 s39, s49, 0
	v_readlane_b32 s41, v237, 34
	s_add_u32 s40, s48, 0x5000
	v_readlane_b32 s42, v237, 35
	s_addc_u32 s41, s49, 0
	v_readlane_b32 s43, v237, 36
	s_add_u32 s42, s48, 0x5100
	v_readlane_b32 s44, v237, 37
	s_addc_u32 s43, s49, 0
	v_readlane_b32 s45, v237, 38
	s_add_u32 s44, s48, 0x5200
	v_readlane_b32 s46, v237, 39
	s_addc_u32 s45, s49, 0
	v_readlane_b32 s47, v237, 40
	s_add_u32 s46, s48, 0x5300
	s_addc_u32 s47, s49, 0
	s_mov_b32 s54, 1
	v_mov_b32_e32 v17, 0
	v_readlane_b32 s50, v237, 43
	v_readlane_b32 s51, v237, 44
	s_branch .LBB0_941

.LBB0_1005:
	v_readlane_b32 s1, v236, 34
	s_cmpk_gt_i32 s1, 0x1ff
	s_mov_b32 s80, 0
	s_waitcnt vmcnt(0)
	s_barrier
	v_writelane_b32 v239, s4, 0
	v_writelane_b32 v239, s12, 1
	v_writelane_b32 v239, s24, 2
	v_writelane_b32 v239, s26, 3
	v_writelane_b32 v239, s30, 4
	v_writelane_b32 v239, s56, 5
	v_writelane_b32 v239, s57, 6
	s_mov_b32 s32, 1
	s_branch .Lmemkv_entry
.Lmemkv_ret:
	s_mov_b32 s32, 0
	v_readlane_b32 s4, v239, 0
	v_readlane_b32 s12, v239, 1
	v_readlane_b32 s24, v239, 2
	v_readlane_b32 s26, v239, 3
	v_readlane_b32 s30, v239, 4
	v_readlane_b32 s56, v239, 5
	v_readlane_b32 s57, v239, 6
	v_and_b32_e32 v156, 31, v0
	v_readlane_b32 s1, v236, 34
	s_nop 1
	s_cmpk_gt_i32 s1, 0x1ff
	s_cbranch_scc1 .LBB0_1007
	s_abs_i32 s0, s82
	v_cvt_f32_u32_e32 v1, s0
	s_sub_i32 s1, s82, s1
	s_add_i32 s2, s1, 0x1ff
	s_sub_i32 s1, 0xfffffe01, s1
	v_rcp_iflag_f32_e32 v1, v1
	s_xor_b32 s4, s2, s82
	s_sub_i32 s3, 0, s0
	s_max_i32 s1, s2, s1
	v_mul_f32_e32 v1, 0x4f7ffffe, v1
	v_cvt_u32_f32_e32 v1, v1
	s_ashr_i32 s2, s4, 31
	v_readfirstlane_b32 s4, v1
	s_mul_i32 s3, s3, s4
	s_mul_hi_u32 s3, s4, s3
	s_add_i32 s4, s4, s3
	s_mul_hi_u32 s3, s1, s4
	s_mul_i32 s4, s3, s0
	s_sub_i32 s1, s1, s4
	s_add_i32 s5, s3, 1
	s_sub_i32 s4, s1, s0
	s_cmp_ge_u32 s1, s0
	s_cselect_b32 s3, s5, s3
	s_cselect_b32 s1, s4, s1
	s_add_i32 s4, s3, 1
	s_cmp_ge_u32 s1, s0
	s_cselect_b32 s0, s4, s3
	s_xor_b32 s0, s0, s2
	s_sub_i32 s0, s0, s2
	s_lshl_b32 s80, s0, 1

.LBB0_1010:
	s_lshr_b32 s4, s94, 1
	s_mul_i32 s4, s4, s82
	v_readlane_b32 s5, v236, 34
	s_add_i32 s5, s4, s5
	s_and_b32 s4, s5, 7
	s_ashr_i32 s6, s5, 5
	s_lshl_b32 s5, s5, 5
	s_and_b32 s6, s6, -8
	s_and_b32 s5, s5, 0x1f00
	s_or_b32 s4, s6, s4
	s_and_b32 s6, s94, 1
	s_xor_b32 s7, s5, 0x3f00
	v_readlane_b32 s12, v237, 61
	s_cmp_eq_u32 s6, 0
	v_readlane_b32 s13, v237, 62
	v_readlane_b32 s14, v237, 63
	v_readlane_b32 s15, v238, 0
	v_readlane_b32 s16, v238, 1
	v_readlane_b32 s17, v238, 2
	v_readlane_b32 s18, v238, 3
	v_readlane_b32 s19, v238, 4
	v_readlane_b32 s20, v238, 5
	v_readlane_b32 s21, v238, 6
	v_readlane_b32 s22, v238, 7
	v_readlane_b32 s23, v238, 8
	s_cselect_b32 s8, s5, s7
	v_readlane_b32 s24, v238, 9
	v_readlane_b32 s25, v238, 10
	v_readlane_b32 s26, v238, 11
	v_readlane_b32 s27, v238, 12
	s_mov_b64 s[12:13], s[16:17]
	s_lshl_b32 s97, s8, 11
	s_mov_b64 s[14:15], s[18:19]
	s_mov_b64 s[16:17], s[20:21]
	s_mov_b64 s[18:19], s[22:23]
	s_add_u32 s5, s18, s97
	s_addc_u32 s6, s19, 0
	s_lshl_b32 s66, s4, 7
	s_ashr_i32 s67, s66, 31
	s_add_u32 s9, s5, s66
	s_mov_b64 s[20:21], s[24:25]
	s_addc_u32 s10, s6, s67
	s_lshl_b32 s5, s8, 10
	s_add_u32 s5, s20, s5
	s_addc_u32 s6, s21, 0
	s_lshl_b32 s7, s4, 6
	s_ashr_i32 s11, s7, 31
	s_add_u32 s12, s5, s7
	s_mov_b64 s[22:23], s[26:27]
	s_addc_u32 s11, s6, s11
	s_add_u32 s6, s22, s66
	s_addc_u32 s7, s23, s67
	s_ashr_i32 s5, s4, 31
	s_lshl_b64 s[4:5], s[4:5], 21
	s_add_u32 s4, s84, s4
	v_readfirstlane_b32 s13, v0
	s_addc_u32 s5, s85, s5
	s_lshr_b32 s14, s13, 6
	s_lshl_b32 s70, s14, 5
	s_lshr_b32 s72, s8, 6
	s_add_i32 s95, s70, s8
	s_and_b32 s8, s13, 0x3fffffc0
	s_lshl_b32 s8, s8, 2
	s_add_i32 s8, s8, 0
	s_add_i32 s13, s8, 0x14000
	s_add_i32 s72, s72, 4
	s_lshl_b32 s74, s14, 10
	s_cmp_lg_u32 0, -1
	s_cselect_b32 s8, 0, 0
	s_add_i32 s73, s74, s8
	s_cmp_lg_u32 s81, -1
	s_cselect_b32 s8, s81, 0
	v_or_b32_e32 v6, s74, v206
	s_add_i32 s74, s74, s8
	s_add_i32 s75, s74, 0x8000
	s_lshl_b64 s[92:93], s[70:71], 11
	s_add_u32 s8, s9, s92
	s_addc_u32 s9, s10, s93
	v_lshl_add_u64 v[8:9], s[8:9], 0, v[158:159]
	s_lshl_b64 s[8:9], s[70:71], 10
	s_add_u32 s8, s12, s8
	s_addc_u32 s9, s11, s9
	v_lshl_add_u64 v[8:9], v[8:9], 0, v[160:161]
	v_lshl_add_u64 v[10:11], s[8:9], 0, v[162:163]
	v_lshl_add_u64 v[10:11], v[10:11], 0, v[160:161]
	global_load_dwordx4 v[100:103], v[8:9], off
	global_load_dwordx4 v[104:107], v[8:9], off offset:32
	global_load_dwordx4 v[108:111], v[8:9], off offset:64
	global_load_dwordx4 v[112:115], v[8:9], off offset:96
	global_load_dwordx4 v[116:119], v[10:11], off
	global_load_dwordx4 v[120:123], v[10:11], off offset:32
	v_lshl_or_b32 v4, s14, 3, v205
	v_lshrrev_b32_e32 v2, 1, v4
	v_xor_b32_e32 v2, v2, v0
	v_lshlrev_b32_e32 v2, 4, v2
	v_and_b32_e32 v5, 0x70, v2
	v_lshl_or_b32 v2, v4, 11, v5
	v_lshl_or_b32 v4, v4, 7, v5
	v_lshl_add_u64 v[8:9], s[6:7], 0, v[2:3]
	s_mov_b32 s6, m0
	s_mov_b32 m0, s74
	s_nop 0
	global_load_lds_dwordx4 v[8:9], off
	s_mov_b32 m0, s6
	v_mov_b32_e32 v5, v3
	v_lshl_add_u64 v[4:5], s[16:17], 0, v[4:5]
	s_mov_b32 s6, m0
	s_mov_b32 m0, s75
	s_nop 0
	global_load_lds_dwordx4 v[4:5], off
	s_mov_b32 m0, s6
	v_mov_b32_e32 v7, v3
	v_lshl_add_u64 v[6:7], s[4:5], 0, v[6:7]
	s_mov_b32 s4, m0
	s_mov_b32 m0, s73
	s_nop 0
	global_load_lds_dwordx4 v[6:7], off
	s_mov_b32 m0, s4
	v_mov_b32_e32 v16, v3
	v_mov_b32_e32 v17, v3
	s_waitcnt vmcnt(0) lgkmcnt(0)
	s_barrier
	v_lshl_add_u64 v[194:195], v[8:9], 0, s[88:89]
	v_lshl_add_u64 v[196:197], v[4:5], 0, s[68:69]
	v_lshl_add_u64 v[198:199], v[6:7], 0, s[68:69]
	v_mov_b32_e32 v2, v3
	v_mov_b32_e32 v4, v3
	v_mov_b32_e32 v5, v3
	v_mov_b32_e32 v6, v3
	v_mov_b32_e32 v7, v3
	v_mov_b32_e32 v8, v3
	v_mov_b32_e32 v9, v3
	v_mov_b32_e32 v10, v3
	v_mov_b32_e32 v11, v3
	v_mov_b32_e32 v12, v3
	v_mov_b32_e32 v13, v3
	v_mov_b32_e32 v14, v3
	v_mov_b32_e32 v15, v3
	v_mov_b64_e32 v[66:67], v[16:17]
	v_mov_b64_e32 v[50:51], v[16:17]
	v_mov_b64_e32 v[34:35], v[16:17]
	v_mov_b64_e32 v[64:65], v[14:15]
	v_mov_b64_e32 v[62:63], v[12:13]
	v_mov_b64_e32 v[60:61], v[10:11]
	v_mov_b64_e32 v[58:59], v[8:9]
	v_mov_b64_e32 v[56:57], v[6:7]
	v_mov_b64_e32 v[54:55], v[4:5]
	v_mov_b64_e32 v[52:53], v[2:3]
	v_mov_b64_e32 v[48:49], v[14:15]
	v_mov_b64_e32 v[46:47], v[12:13]
	v_mov_b64_e32 v[44:45], v[10:11]
	v_mov_b64_e32 v[42:43], v[8:9]
	v_mov_b64_e32 v[40:41], v[6:7]
	v_mov_b64_e32 v[38:39], v[4:5]
	v_mov_b64_e32 v[36:37], v[2:3]
	v_mov_b64_e32 v[32:33], v[14:15]
	v_mov_b64_e32 v[30:31], v[12:13]
	v_mov_b64_e32 v[28:29], v[10:11]
	v_mov_b64_e32 v[26:27], v[8:9]
	v_mov_b64_e32 v[24:25], v[6:7]
	v_mov_b64_e32 v[22:23], v[4:5]
	v_mov_b64_e32 v[20:21], v[2:3]
	v_mov_b64_e32 v[18:19], v[16:17]
	s_or_b32 s70, s95, 31
	v_lshl_add_u32 v214, v156, 2, s13
	v_lshl_add_u32 v213, v204, 2, s13
	v_add_u32_e32 v215, s95, v209
	v_mov_b32_e32 v216, 0xf149f2ca
	s_mov_b32 s76, 63
	v_mov_b64_e32 v[16:17], v[14:15]
	v_mov_b64_e32 v[14:15], v[12:13]
	v_mov_b64_e32 v[12:13], v[10:11]
	v_mov_b64_e32 v[10:11], v[8:9]
	v_mov_b64_e32 v[8:9], v[6:7]
	v_mov_b64_e32 v[6:7], v[4:5]
	v_mov_b64_e32 v[4:5], v[2:3]
	s_mov_b32 s77, 0
	v_mov_b32_e32 v2, 0
	s_mov_b32 s40, m0
	s_lshr_b32 s4, s70, 6
	s_add_i32 s4, s4, 1
	s_min_u32 s42, s4, s72
	s_lshr_b32 s43, s95, 6
	v_add_u32_e32 v242, 0x10000, v200
	v_add_u32_e32 v243, 0x10000, v201
	v_readlane_b32 s37, v236, 34
	v_readfirstlane_b32 s4, v0
	s_nop 3
	s_lshr_b32 s36, s4, 6
	s_sub_i32 s37, s37, 4
	s_mov_b32 s50, 0x44000000
	s_mov_b32 s51, 0x44000000
	s_mov_b32 s47, 0
	s_mov_b32 s48, 0
	v_and_b32_e32 v241, 63, v0
	v_lshlrev_b32_e32 v240, 11, v241
	v_lshlrev_b32_e32 v241, 2, v241
	v_mov_b32_e32 v217, 1.0
	v_mov_b32_e32 v218, 0x38383838
	v_mov_b32_e32 v219, 0x38383838
	v_mov_b32_e32 v220, 0x38383838
	v_mov_b32_e32 v221, 0x38383838
	v_mov_b32_e32 v222, 0x38383838
	v_mov_b32_e32 v223, 0x38383838
	v_mov_b32_e32 v224, 0x38383838
	v_mov_b32_e32 v225, 0x38383838
	s_cmp_ge_u32 s36, 4
	s_cbranch_scc1 .Lm_Lstart

.Lm_nd1:
	ds_read_b128 v[166:169], v200 offset:32768
	ds_read_b128 v[170:173], v201 offset:32768
	ds_read_b128 v[174:177], v200 offset:36864
	ds_read_b128 v[178:181], v201 offset:36864
	ds_read_b128 v[182:185], v202 offset:32768
	ds_read_b128 v[186:189], v203 offset:32768
	s_waitcnt lgkmcnt(4)
	v_mfma_f32_32x32x64_f8f6f4 v[68:83], v[166:173], v[100:107], 0
	ds_read_b128 v[166:169], v202 offset:36864
	ds_read_b128 v[170:173], v203 offset:36864
	s_waitcnt lgkmcnt(4)
	v_mfma_f32_32x32x64_f8f6f4 v[84:99], v[174:181], v[100:107], 0
	ds_read_b128 v[174:177], v242 offset:0
	ds_read_b128 v[178:181], v243 offset:0
	s_waitcnt lgkmcnt(4)
	v_mfma_f32_32x32x64_f8f6f4 v[68:83], v[182:189], v[108:115], v[68:83]
	ds_read_b128 v[182:185], v242 offset:4096
	ds_read_b128 v[186:189], v243 offset:4096
	s_waitcnt lgkmcnt(4)
	v_mfma_f32_32x32x64_f8f6f4 v[84:99], v[166:173], v[108:115], v[84:99]
	s_waitcnt lgkmcnt(2)
	v_mfma_f32_32x32x64_f8f6f4 v[68:83], v[174:181], v[116:123], v[68:83]
	s_waitcnt lgkmcnt(0)
	v_mfma_f32_32x32x64_f8f6f4 v[84:99], v[182:189], v[116:123], v[84:99]
	s_waitcnt vmcnt(0) lgkmcnt(0)
	s_cmp_eq_u32 s48, 0
	s_cbranch_scc1 .Lm_bf3
	v_pk_mul_f32 v[226:227], v[226:227], s[50:51]
	v_pk_mul_f32 v[228:229], v[228:229], s[50:51]
	v_pk_mul_f32 v[230:231], v[230:231], s[50:51]
	v_pk_mul_f32 v[232:233], v[232:233], s[50:51]
	v_med3_f32 v226, v226, s33, v212
	v_med3_f32 v227, v227, s33, v212
	v_med3_f32 v228, v228, s33, v212
	v_med3_f32 v229, v229, s33, v212
	v_med3_f32 v230, v230, s33, v212
	v_med3_f32 v231, v231, s33, v212
	v_med3_f32 v232, v232, s33, v212
	v_med3_f32 v233, v233, s33, v212
	v_cvt_pk_fp8_f32 v246, v226, v227
	v_cvt_pk_fp8_f32 v247, v230, v231
	v_cvt_pk_fp8_f32 v246, v228, v229 op_sel:[0,0,1]
	v_cvt_pk_fp8_f32 v247, v232, v233 op_sel:[0,0,1]
	global_store_dwordx4 v240, v[244:247], s[44:45]
	s_mov_b32 s48, 0
.Lm_bf3:
	s_cmp_lt_i32 s37, 0
	s_cbranch_scc1 .Lm_bs2
	s_mul_i32 s4, s83, 252
	s_add_i32 s4, s4, s37
	s_cmp_ge_u32 s4, 0xc000
	s_cbranch_scc1 .Lm_bs2
	s_cmp_ge_u32 s4, 0x8000
	s_cbranch_scc1 .Lm_dn4
	s_lshr_b32 s5, s4, 10
	s_bfe_u32 s6, s4, 0x40006
	s_and_b32 s7, s4, 63
	s_lshl_b32 s8, s6, 7
	s_lshl_b32 s9, s36, 4
	s_add_i32 s8, s8, s9
	s_lshl_b32 s10, s5, 25
	s_lshl_b32 s11, s8, 14
	s_add_i32 s10, s10, s11
	s_lshl_b32 s11, s7, 8
	s_add_i32 s10, s10, s11
	v_readlane_b32 s14, v237, 29
	v_readlane_b32 s15, v237, 30
	s_add_u32 s14, s14, s10
	s_addc_u32 s15, s15, 0
	s_mov_b32 s46, 0x4000
	s_bfe_u32 s10, s7, 0x40001
	s_lshl_b32 s10, s10, 8
	s_and_b32 s11, s7, 1
	s_lshl_b32 s11, s11, 6
	s_add_i32 s10, s10, s11
	s_lshr_b32 s11, s7, 5
	s_lshl_b32 s11, s11, 7
	s_add_i32 s10, s10, s11
	s_lshl_b32 s10, s10, 11
	s_add_i32 s10, s10, s8
	s_lshl_b32 s11, s5, 23
	s_add_i32 s10, s10, s11
	v_readlane_b32 s44, v237, 51
	v_readlane_b32 s45, v237, 52
	s_add_u32 s44, s44, s10
	s_addc_u32 s45, s45, 0
	s_branch .Lm_dd4

.Lm_nr8:
	v_fmamk_f32 v190, v216, 0xbad53b94, v210
	v_fma_f32 v68, v68, s96, v190
	v_fma_f32 v69, v69, s96, v190
	v_fma_f32 v84, v84, s96, v190
	v_fma_f32 v85, v85, s96, v190
	v_fma_f32 v70, v70, s96, v190
	v_fma_f32 v71, v71, s96, v190
	v_fma_f32 v86, v86, s96, v190
	v_fma_f32 v87, v87, s96, v190
	v_fma_f32 v72, v72, s96, v190
	v_fma_f32 v73, v73, s96, v190
	v_fma_f32 v88, v88, s96, v190
	v_fma_f32 v89, v89, s96, v190
	v_fma_f32 v74, v74, s96, v190
	v_fma_f32 v75, v75, s96, v190
	v_fma_f32 v90, v90, s96, v190
	v_fma_f32 v91, v91, s96, v190
	v_fma_f32 v76, v76, s96, v190
	v_fma_f32 v77, v77, s96, v190
	v_fma_f32 v92, v92, s96, v190
	v_fma_f32 v93, v93, s96, v190
	v_fma_f32 v78, v78, s96, v190
	v_fma_f32 v79, v79, s96, v190
	v_fma_f32 v94, v94, s96, v190
	v_fma_f32 v95, v95, s96, v190
	v_fma_f32 v80, v80, s96, v190
	v_fma_f32 v81, v81, s96, v190
	v_fma_f32 v96, v96, s96, v190
	v_fma_f32 v97, v97, s96, v190
	v_fma_f32 v82, v82, s96, v190
	v_fma_f32 v83, v83, s96, v190
	v_fma_f32 v98, v98, s96, v190
	v_fma_f32 v99, v99, s96, v190
	v_exp_f32_e32 v68, v68
	v_exp_f32_e32 v69, v69
	v_exp_f32_e32 v70, v70
	v_exp_f32_e32 v71, v71
	v_exp_f32_e32 v72, v72
	v_exp_f32_e32 v73, v73
	v_exp_f32_e32 v74, v74
	v_exp_f32_e32 v75, v75
	v_exp_f32_e32 v76, v76
	v_exp_f32_e32 v77, v77
	v_exp_f32_e32 v78, v78
	v_exp_f32_e32 v79, v79
	v_exp_f32_e32 v80, v80
	v_exp_f32_e32 v81, v81
	v_exp_f32_e32 v82, v82
	v_exp_f32_e32 v83, v83
	v_exp_f32_e32 v84, v84
	v_exp_f32_e32 v85, v85
	v_exp_f32_e32 v86, v86
	v_exp_f32_e32 v87, v87
	v_exp_f32_e32 v88, v88
	v_exp_f32_e32 v89, v89
	v_exp_f32_e32 v90, v90
	v_exp_f32_e32 v91, v91
	v_exp_f32_e32 v92, v92
	v_exp_f32_e32 v93, v93
	v_exp_f32_e32 v94, v94
	v_exp_f32_e32 v95, v95
	v_exp_f32_e32 v96, v96
	v_exp_f32_e32 v97, v97
	v_exp_f32_e32 v98, v98
	v_exp_f32_e32 v99, v99
	ds_read_b128 v[166:169], v200 offset:49152
	ds_read_b128 v[170:173], v201 offset:49152
	ds_read_b128 v[174:177], v200 offset:53248
	ds_read_b128 v[178:181], v201 offset:53248
	ds_read_b128 v[182:185], v202 offset:49152
	ds_read_b128 v[186:189], v203 offset:49152
	s_waitcnt lgkmcnt(4)
	v_mfma_f32_32x32x64_f8f6f4 v[124:139], v[166:173], v[100:107], 0
	ds_read_b128 v[166:169], v202 offset:53248
	ds_read_b128 v[170:173], v203 offset:53248
	s_waitcnt lgkmcnt(4)
	v_mfma_f32_32x32x64_f8f6f4 v[140:155], v[174:181], v[100:107], 0
	ds_read_b128 v[174:177], v242 offset:8192
	ds_read_b128 v[178:181], v243 offset:8192
	s_waitcnt lgkmcnt(4)
	v_mfma_f32_32x32x64_f8f6f4 v[124:139], v[182:189], v[108:115], v[124:139]
	ds_read_b128 v[182:185], v242 offset:12288
	ds_read_b128 v[186:189], v243 offset:12288
	s_waitcnt lgkmcnt(4)
	v_mfma_f32_32x32x64_f8f6f4 v[140:155], v[166:173], v[108:115], v[140:155]
	s_waitcnt lgkmcnt(2)
	v_mfma_f32_32x32x64_f8f6f4 v[124:139], v[174:181], v[116:123], v[124:139]
	s_waitcnt lgkmcnt(0)
	v_mfma_f32_32x32x64_f8f6f4 v[140:155], v[182:189], v[116:123], v[140:155]
	s_branch .Lm_p1e6

.Lm_p1e6:
	v_cvt_pk_fp8_f32 v248, v68, v69
	v_cvt_pk_fp8_f32 v249, v72, v73
	v_cvt_pk_fp8_f32 v250, v76, v77
	v_cvt_pk_fp8_f32 v251, v80, v81
	v_cvt_pk_fp8_f32 v252, v84, v85
	v_cvt_pk_fp8_f32 v253, v88, v89
	v_cvt_pk_fp8_f32 v254, v92, v93
	v_cvt_pk_fp8_f32 v255, v96, v97
	v_cvt_pk_fp8_f32 v248, v70, v71 op_sel:[0,0,1]
	v_cvt_pk_fp8_f32 v249, v74, v75 op_sel:[0,0,1]
	v_cvt_pk_fp8_f32 v250, v78, v79 op_sel:[0,0,1]
	v_cvt_pk_fp8_f32 v251, v82, v83 op_sel:[0,0,1]
	v_cvt_pk_fp8_f32 v252, v86, v87 op_sel:[0,0,1]
	v_cvt_pk_fp8_f32 v253, v90, v91 op_sel:[0,0,1]
	v_cvt_pk_fp8_f32 v254, v94, v95 op_sel:[0,0,1]
	v_cvt_pk_fp8_f32 v255, v98, v99 op_sel:[0,0,1]
	s_nop 1
	v_mfma_f32_32x32x64_f8f6f4 v[68:83], v[218:225], v[248:255], 0
	s_waitcnt vmcnt(0) lgkmcnt(0)
	s_cmp_eq_u32 s48, 0
	s_cbranch_scc1 .Lm_bi11
	v_pk_mul_f32 v[226:227], v[226:227], s[50:51]
	v_pk_mul_f32 v[228:229], v[228:229], s[50:51]
	v_pk_mul_f32 v[230:231], v[230:231], s[50:51]
	v_pk_mul_f32 v[232:233], v[232:233], s[50:51]
	v_med3_f32 v226, v226, s33, v212
	v_med3_f32 v227, v227, s33, v212
	v_med3_f32 v228, v228, s33, v212
	v_med3_f32 v229, v229, s33, v212
	v_med3_f32 v230, v230, s33, v212
	v_med3_f32 v231, v231, s33, v212
	v_med3_f32 v232, v232, s33, v212
	v_med3_f32 v233, v233, s33, v212
	v_cvt_pk_fp8_f32 v244, v226, v227
	v_cvt_pk_fp8_f32 v245, v230, v231
	v_cvt_pk_fp8_f32 v244, v228, v229 op_sel:[0,0,1]
	v_cvt_pk_fp8_f32 v245, v232, v233 op_sel:[0,0,1]
	global_load_dword v226, v241, s[14:15]
	s_add_u32 s14, s14, s46
	s_addc_u32 s15, s15, 0
	global_load_dword v227, v241, s[14:15]
	s_add_u32 s14, s14, s46
	s_addc_u32 s15, s15, 0
	global_load_dword v228, v241, s[14:15]
	s_add_u32 s14, s14, s46
	s_addc_u32 s15, s15, 0
	global_load_dword v229, v241, s[14:15]
	s_add_u32 s14, s14, s46
	s_addc_u32 s15, s15, 0
	global_load_dword v230, v241, s[14:15]
	s_add_u32 s14, s14, s46
	s_addc_u32 s15, s15, 0
	global_load_dword v231, v241, s[14:15]
	s_add_u32 s14, s14, s46
	s_addc_u32 s15, s15, 0
	global_load_dword v232, v241, s[14:15]
	s_add_u32 s14, s14, s46
	s_addc_u32 s15, s15, 0
	global_load_dword v233, v241, s[14:15]
	s_add_u32 s14, s14, s46
	s_addc_u32 s15, s15, 0

.Lm_nm14:
	ds_read_b128 v[166:169], v207 offset:0
	ds_read_b128 v[170:173], v208 offset:0
	ds_read_b128 v[174:177], v207 offset:2048
	ds_read_b128 v[178:181], v208 offset:2048
	ds_read_b128 v[182:185], v207 offset:4096
	ds_read_b128 v[186:189], v208 offset:4096
	s_waitcnt lgkmcnt(4)
	v_mfma_f32_32x32x64_f8f6f4 v[52:67], v[248:255], v[166:173], v[52:67]
	ds_read_b128 v[166:169], v207 offset:6144
	ds_read_b128 v[170:173], v208 offset:6144
	v_max3_f32 v239, v124, v125, v126
	v_max3_f32 v235, v140, v141, v142
	v_max3_f32 v239, v239, v127, v128
	v_max3_f32 v235, v235, v143, v144
	v_max3_f32 v239, v239, v129, v130
	s_waitcnt lgkmcnt(4)
	v_mfma_f32_32x32x64_f8f6f4 v[36:51], v[248:255], v[174:181], v[36:51]
	ds_read_b128 v[174:177], v200 offset:40960
	ds_read_b128 v[178:181], v201 offset:40960
	v_max3_f32 v235, v235, v145, v146
	v_max3_f32 v239, v239, v131, v132
	v_max3_f32 v235, v235, v147, v148
	v_max3_f32 v239, v239, v133, v134
	v_max3_f32 v235, v235, v149, v150
	v_fma_f32 v2, v2, v217, v68
	v_mov_b32_e32 v217, 1.0
	s_waitcnt lgkmcnt(4)
	v_mfma_f32_32x32x64_f8f6f4 v[20:35], v[248:255], v[182:189], v[20:35]
	ds_read_b128 v[182:185], v200 offset:45056
	ds_read_b128 v[186:189], v201 offset:45056
	v_max3_f32 v239, v239, v135, v136
	v_max3_f32 v235, v235, v151, v152
	v_max3_f32 v239, v239, v137, v138
	v_max3_f32 v235, v235, v153, v154
	s_waitcnt lgkmcnt(4)
	v_mfma_f32_32x32x64_f8f6f4 v[4:19], v[248:255], v[166:173], v[4:19]
	ds_read_b128 v[166:169], v202 offset:40960
	ds_read_b128 v[170:173], v203 offset:40960
	v_max3_f32 v239, v239, v139, v155
	v_max_f32_e32 v239, v239, v235
	v_mov_b32_e32 v234, v239
	s_waitcnt lgkmcnt(4)
	v_mfma_f32_32x32x64_f8f6f4 v[68:83], v[174:181], v[100:107], 0
	ds_read_b128 v[174:177], v202 offset:45056
	ds_read_b128 v[178:181], v203 offset:45056
	s_nop 1
	v_permlane32_swap_b32_e32 v239, v234
	v_max_f32_e32 v239, v239, v234
	v_sub_f32_e32 v235, v239, v216
	v_mul_f32_e32 v235, 0x3a93cd3a, v235
	v_cmp_ge_f32_e32 vcc, 2.0, v235
	s_cmp_eq_u64 vcc, exec
	s_cbranch_scc1 .Lm_nr15
	v_max_f32_e32 v235, v216, v239
	v_sub_f32_e32 v217, v216, v235
	v_mul_f32_e32 v217, 0x3ad53b94, v217
	v_exp_f32_e32 v217, v217
	v_mov_b32_e32 v216, v235
	s_and_saveexec_b64 s[6:7], s[0:1]
	ds_write_b32 v214, v217 offset:128
	s_or_b64 exec, exec, s[6:7]
	s_waitcnt lgkmcnt(0)
	ds_read_b128 v[84:87], v213 offset:128
	s_waitcnt lgkmcnt(0)
	v_pk_mul_f32 v[52:53], v[52:53], v[84:85]
	v_pk_mul_f32 v[54:55], v[54:55], v[86:87]
	v_pk_mul_f32 v[36:37], v[36:37], v[84:85]
	v_pk_mul_f32 v[38:39], v[38:39], v[86:87]
	v_pk_mul_f32 v[20:21], v[20:21], v[84:85]
	v_pk_mul_f32 v[22:23], v[22:23], v[86:87]
	v_pk_mul_f32 v[4:5], v[4:5], v[84:85]
	v_pk_mul_f32 v[6:7], v[6:7], v[86:87]
	ds_read_b128 v[84:87], v213 offset:160
	s_waitcnt lgkmcnt(0)
	v_pk_mul_f32 v[56:57], v[56:57], v[84:85]
	v_pk_mul_f32 v[58:59], v[58:59], v[86:87]
	v_pk_mul_f32 v[40:41], v[40:41], v[84:85]
	v_pk_mul_f32 v[42:43], v[42:43], v[86:87]
	v_pk_mul_f32 v[24:25], v[24:25], v[84:85]
	v_pk_mul_f32 v[26:27], v[26:27], v[86:87]
	v_pk_mul_f32 v[8:9], v[8:9], v[84:85]
	v_pk_mul_f32 v[10:11], v[10:11], v[86:87]
	ds_read_b128 v[84:87], v213 offset:192
	s_waitcnt lgkmcnt(0)
	v_pk_mul_f32 v[60:61], v[60:61], v[84:85]
	v_pk_mul_f32 v[62:63], v[62:63], v[86:87]
	v_pk_mul_f32 v[44:45], v[44:45], v[84:85]
	v_pk_mul_f32 v[46:47], v[46:47], v[86:87]
	v_pk_mul_f32 v[28:29], v[28:29], v[84:85]
	v_pk_mul_f32 v[30:31], v[30:31], v[86:87]
	v_pk_mul_f32 v[12:13], v[12:13], v[84:85]
	v_pk_mul_f32 v[14:15], v[14:15], v[86:87]
	ds_read_b128 v[84:87], v213 offset:224
	s_waitcnt lgkmcnt(0)
	v_pk_mul_f32 v[64:65], v[64:65], v[84:85]
	v_pk_mul_f32 v[66:67], v[66:67], v[86:87]
	v_pk_mul_f32 v[48:49], v[48:49], v[84:85]
	v_pk_mul_f32 v[50:51], v[50:51], v[86:87]
	v_pk_mul_f32 v[32:33], v[32:33], v[84:85]
	v_pk_mul_f32 v[34:35], v[34:35], v[86:87]
	v_pk_mul_f32 v[16:17], v[16:17], v[84:85]
	v_pk_mul_f32 v[18:19], v[18:19], v[86:87]
.Lm_nr15:
	v_fmamk_f32 v190, v216, 0xbad53b94, v210
	v_fma_f32 v124, v124, s96, v190
	v_fma_f32 v125, v125, s96, v190
	v_fma_f32 v140, v140, s96, v190
	v_fma_f32 v141, v141, s96, v190
	v_fma_f32 v126, v126, s96, v190
	v_fma_f32 v127, v127, s96, v190
	v_fma_f32 v142, v142, s96, v190
	v_fma_f32 v143, v143, s96, v190
	v_fma_f32 v128, v128, s96, v190
	v_fma_f32 v129, v129, s96, v190
	v_fma_f32 v144, v144, s96, v190
	v_fma_f32 v145, v145, s96, v190
	v_fma_f32 v130, v130, s96, v190
	v_fma_f32 v131, v131, s96, v190
	v_fma_f32 v146, v146, s96, v190
	v_fma_f32 v147, v147, s96, v190
	v_fma_f32 v132, v132, s96, v190
	s_waitcnt lgkmcnt(4)
	v_mfma_f32_32x32x64_f8f6f4 v[84:99], v[182:189], v[100:107], 0
	ds_read_b128 v[182:185], v242 offset:32768
	ds_read_b128 v[186:189], v243 offset:32768
	v_fma_f32 v133, v133, s96, v190
	v_fma_f32 v148, v148, s96, v190
	v_fma_f32 v149, v149, s96, v190
	v_fma_f32 v134, v134, s96, v190
	v_fma_f32 v135, v135, s96, v190
	v_fma_f32 v150, v150, s96, v190
	v_fma_f32 v151, v151, s96, v190
	v_fma_f32 v136, v136, s96, v190
	v_fma_f32 v137, v137, s96, v190
	v_fma_f32 v152, v152, s96, v190
	v_fma_f32 v153, v153, s96, v190
	v_fma_f32 v138, v138, s96, v190
	v_fma_f32 v139, v139, s96, v190
	v_fma_f32 v154, v154, s96, v190
	v_fma_f32 v155, v155, s96, v190
	v_exp_f32_e32 v124, v124
	v_exp_f32_e32 v125, v125
	v_exp_f32_e32 v126, v126
	s_waitcnt lgkmcnt(4)
	v_mfma_f32_32x32x64_f8f6f4 v[68:83], v[166:173], v[108:115], v[68:83]
	ds_read_b128 v[166:169], v242 offset:36864
	ds_read_b128 v[170:173], v243 offset:36864
	v_exp_f32_e32 v127, v127
	v_exp_f32_e32 v128, v128
	v_exp_f32_e32 v129, v129
	v_exp_f32_e32 v130, v130
	v_exp_f32_e32 v131, v131
	v_exp_f32_e32 v132, v132
	v_exp_f32_e32 v133, v133
	s_waitcnt lgkmcnt(4)
	v_mfma_f32_32x32x64_f8f6f4 v[84:99], v[174:181], v[108:115], v[84:99]
	v_exp_f32_e32 v134, v134
	v_exp_f32_e32 v135, v135
	v_exp_f32_e32 v136, v136
	v_exp_f32_e32 v137, v137
	v_exp_f32_e32 v138, v138
	v_exp_f32_e32 v139, v139
	v_exp_f32_e32 v140, v140
	v_exp_f32_e32 v141, v141
	s_waitcnt lgkmcnt(2)
	v_mfma_f32_32x32x64_f8f6f4 v[68:83], v[182:189], v[116:123], v[68:83]
	v_exp_f32_e32 v142, v142
	v_exp_f32_e32 v143, v143
	v_exp_f32_e32 v144, v144
	v_exp_f32_e32 v145, v145
	v_exp_f32_e32 v146, v146
	v_exp_f32_e32 v147, v147
	v_exp_f32_e32 v148, v148
	s_waitcnt lgkmcnt(0)
	v_mfma_f32_32x32x64_f8f6f4 v[84:99], v[166:173], v[116:123], v[84:99]
	v_exp_f32_e32 v149, v149
	v_exp_f32_e32 v150, v150
	v_exp_f32_e32 v151, v151
	v_exp_f32_e32 v152, v152
	v_exp_f32_e32 v153, v153
	v_exp_f32_e32 v154, v154
	v_exp_f32_e32 v155, v155
.Lm_m13_end:
	s_sub_i32 s5, s77, 1
	s_cmp_ge_u32 s5, s42
	s_cbranch_scc1 .Lm_t16_end
	v_cvt_pk_fp8_f32 v248, v124, v125
	v_cvt_pk_fp8_f32 v249, v128, v129
	v_cvt_pk_fp8_f32 v250, v132, v133
	v_cvt_pk_fp8_f32 v251, v136, v137
	v_cvt_pk_fp8_f32 v252, v140, v141
	v_cvt_pk_fp8_f32 v253, v144, v145
	v_cvt_pk_fp8_f32 v254, v148, v149
	v_cvt_pk_fp8_f32 v255, v152, v153
	v_cvt_pk_fp8_f32 v248, v126, v127 op_sel:[0,0,1]
	v_cvt_pk_fp8_f32 v249, v130, v131 op_sel:[0,0,1]
	v_cvt_pk_fp8_f32 v250, v134, v135 op_sel:[0,0,1]
	v_cvt_pk_fp8_f32 v251, v138, v139 op_sel:[0,0,1]
	v_cvt_pk_fp8_f32 v252, v142, v143 op_sel:[0,0,1]
	v_cvt_pk_fp8_f32 v253, v146, v147 op_sel:[0,0,1]
	v_cvt_pk_fp8_f32 v254, v150, v151 op_sel:[0,0,1]
	v_cvt_pk_fp8_f32 v255, v154, v155 op_sel:[0,0,1]
	s_nop 1
	v_mfma_f32_32x32x64_f8f6f4 v[124:139], v[218:225], v[248:255], 0

.Lm_nm22:
	ds_read_b128 v[166:169], v207 offset:16384
	ds_read_b128 v[170:173], v208 offset:16384
	ds_read_b128 v[174:177], v207 offset:18432
	ds_read_b128 v[178:181], v208 offset:18432
	ds_read_b128 v[182:185], v207 offset:20480
	ds_read_b128 v[186:189], v208 offset:20480
	s_waitcnt lgkmcnt(4)
	v_mfma_f32_32x32x64_f8f6f4 v[52:67], v[248:255], v[166:173], v[52:67]
	ds_read_b128 v[166:169], v207 offset:22528
	ds_read_b128 v[170:173], v208 offset:22528
	v_max3_f32 v239, v68, v69, v70
	v_max3_f32 v235, v84, v85, v86
	v_max3_f32 v239, v239, v71, v72
	v_max3_f32 v235, v235, v87, v88
	v_max3_f32 v239, v239, v73, v74
	s_waitcnt lgkmcnt(4)
	v_mfma_f32_32x32x64_f8f6f4 v[36:51], v[248:255], v[174:181], v[36:51]
	ds_read_b128 v[174:177], v200 offset:57344
	ds_read_b128 v[178:181], v201 offset:57344
	v_max3_f32 v235, v235, v89, v90
	v_max3_f32 v239, v239, v75, v76
	v_max3_f32 v235, v235, v91, v92
	v_max3_f32 v239, v239, v77, v78
	v_max3_f32 v235, v235, v93, v94
	v_fma_f32 v2, v2, v217, v124
	v_mov_b32_e32 v217, 1.0
	s_waitcnt lgkmcnt(4)
	v_mfma_f32_32x32x64_f8f6f4 v[20:35], v[248:255], v[182:189], v[20:35]
	ds_read_b128 v[182:185], v200 offset:61440
	ds_read_b128 v[186:189], v201 offset:61440
	v_max3_f32 v239, v239, v79, v80
	v_max3_f32 v235, v235, v95, v96
	v_max3_f32 v239, v239, v81, v82
	v_max3_f32 v235, v235, v97, v98
	s_waitcnt lgkmcnt(4)
	v_mfma_f32_32x32x64_f8f6f4 v[4:19], v[248:255], v[166:173], v[4:19]
	ds_read_b128 v[166:169], v202 offset:57344
	ds_read_b128 v[170:173], v203 offset:57344
	v_max3_f32 v239, v239, v83, v99
	v_max_f32_e32 v239, v239, v235
	v_mov_b32_e32 v234, v239
	s_waitcnt lgkmcnt(4)
	v_mfma_f32_32x32x64_f8f6f4 v[124:139], v[174:181], v[100:107], 0
	ds_read_b128 v[174:177], v202 offset:61440
	ds_read_b128 v[178:181], v203 offset:61440
	s_nop 1
	v_permlane32_swap_b32_e32 v239, v234
	v_max_f32_e32 v239, v239, v234
	v_sub_f32_e32 v235, v239, v216
	v_mul_f32_e32 v235, 0x3a93cd3a, v235
	v_cmp_ge_f32_e32 vcc, 2.0, v235
	s_cmp_eq_u64 vcc, exec
	s_cbranch_scc1 .Lm_nr23
	v_max_f32_e32 v235, v216, v239
	v_sub_f32_e32 v217, v216, v235
	v_mul_f32_e32 v217, 0x3ad53b94, v217
	v_exp_f32_e32 v217, v217
	v_mov_b32_e32 v216, v235
	s_and_saveexec_b64 s[6:7], s[0:1]
	ds_write_b32 v214, v217 offset:128
	s_or_b64 exec, exec, s[6:7]
	s_waitcnt lgkmcnt(0)
	ds_read_b128 v[140:143], v213 offset:128
	s_waitcnt lgkmcnt(0)
	v_pk_mul_f32 v[52:53], v[52:53], v[140:141]
	v_pk_mul_f32 v[54:55], v[54:55], v[142:143]
	v_pk_mul_f32 v[36:37], v[36:37], v[140:141]
	v_pk_mul_f32 v[38:39], v[38:39], v[142:143]
	v_pk_mul_f32 v[20:21], v[20:21], v[140:141]
	v_pk_mul_f32 v[22:23], v[22:23], v[142:143]
	v_pk_mul_f32 v[4:5], v[4:5], v[140:141]
	v_pk_mul_f32 v[6:7], v[6:7], v[142:143]
	ds_read_b128 v[140:143], v213 offset:160
	s_waitcnt lgkmcnt(0)
	v_pk_mul_f32 v[56:57], v[56:57], v[140:141]
	v_pk_mul_f32 v[58:59], v[58:59], v[142:143]
	v_pk_mul_f32 v[40:41], v[40:41], v[140:141]
	v_pk_mul_f32 v[42:43], v[42:43], v[142:143]
	v_pk_mul_f32 v[24:25], v[24:25], v[140:141]
	v_pk_mul_f32 v[26:27], v[26:27], v[142:143]
	v_pk_mul_f32 v[8:9], v[8:9], v[140:141]
	v_pk_mul_f32 v[10:11], v[10:11], v[142:143]
	ds_read_b128 v[140:143], v213 offset:192
	s_waitcnt lgkmcnt(0)
	v_pk_mul_f32 v[60:61], v[60:61], v[140:141]
	v_pk_mul_f32 v[62:63], v[62:63], v[142:143]
	v_pk_mul_f32 v[44:45], v[44:45], v[140:141]
	v_pk_mul_f32 v[46:47], v[46:47], v[142:143]
	v_pk_mul_f32 v[28:29], v[28:29], v[140:141]
	v_pk_mul_f32 v[30:31], v[30:31], v[142:143]
	v_pk_mul_f32 v[12:13], v[12:13], v[140:141]
	v_pk_mul_f32 v[14:15], v[14:15], v[142:143]
	ds_read_b128 v[140:143], v213 offset:224
	s_waitcnt lgkmcnt(0)
	v_pk_mul_f32 v[64:65], v[64:65], v[140:141]
	v_pk_mul_f32 v[66:67], v[66:67], v[142:143]
	v_pk_mul_f32 v[48:49], v[48:49], v[140:141]
	v_pk_mul_f32 v[50:51], v[50:51], v[142:143]
	v_pk_mul_f32 v[32:33], v[32:33], v[140:141]
	v_pk_mul_f32 v[34:35], v[34:35], v[142:143]
	v_pk_mul_f32 v[16:17], v[16:17], v[140:141]
	v_pk_mul_f32 v[18:19], v[18:19], v[142:143]
.Lm_nr23:
	v_fmamk_f32 v190, v216, 0xbad53b94, v210
	v_fma_f32 v68, v68, s96, v190
	v_fma_f32 v69, v69, s96, v190
	v_fma_f32 v84, v84, s96, v190
	v_fma_f32 v85, v85, s96, v190
	v_fma_f32 v70, v70, s96, v190
	v_fma_f32 v71, v71, s96, v190
	v_fma_f32 v86, v86, s96, v190
	v_fma_f32 v87, v87, s96, v190
	v_fma_f32 v72, v72, s96, v190
	v_fma_f32 v73, v73, s96, v190
	v_fma_f32 v88, v88, s96, v190
	v_fma_f32 v89, v89, s96, v190
	v_fma_f32 v74, v74, s96, v190
	v_fma_f32 v75, v75, s96, v190
	v_fma_f32 v90, v90, s96, v190
	v_fma_f32 v91, v91, s96, v190
	v_fma_f32 v76, v76, s96, v190
	s_waitcnt lgkmcnt(4)
	v_mfma_f32_32x32x64_f8f6f4 v[140:155], v[182:189], v[100:107], 0
	ds_read_b128 v[182:185], v242 offset:40960
	ds_read_b128 v[186:189], v243 offset:40960
	v_fma_f32 v77, v77, s96, v190
	v_fma_f32 v92, v92, s96, v190
	v_fma_f32 v93, v93, s96, v190
	v_fma_f32 v78, v78, s96, v190
	v_fma_f32 v79, v79, s96, v190
	v_fma_f32 v94, v94, s96, v190
	v_fma_f32 v95, v95, s96, v190
	v_fma_f32 v80, v80, s96, v190
	v_fma_f32 v81, v81, s96, v190
	v_fma_f32 v96, v96, s96, v190
	v_fma_f32 v97, v97, s96, v190
	v_fma_f32 v82, v82, s96, v190
	v_fma_f32 v83, v83, s96, v190
	v_fma_f32 v98, v98, s96, v190
	v_fma_f32 v99, v99, s96, v190
	v_exp_f32_e32 v68, v68
	v_exp_f32_e32 v69, v69
	v_exp_f32_e32 v70, v70
	s_waitcnt lgkmcnt(4)
	v_mfma_f32_32x32x64_f8f6f4 v[124:139], v[166:173], v[108:115], v[124:139]
	ds_read_b128 v[166:169], v242 offset:45056
	ds_read_b128 v[170:173], v243 offset:45056
	v_exp_f32_e32 v71, v71
	v_exp_f32_e32 v72, v72
	v_exp_f32_e32 v73, v73
	v_exp_f32_e32 v74, v74
	v_exp_f32_e32 v75, v75
	v_exp_f32_e32 v76, v76
	v_exp_f32_e32 v77, v77
	s_waitcnt lgkmcnt(4)
	v_mfma_f32_32x32x64_f8f6f4 v[140:155], v[174:181], v[108:115], v[140:155]
	v_exp_f32_e32 v78, v78
	v_exp_f32_e32 v79, v79
	v_exp_f32_e32 v80, v80
	v_exp_f32_e32 v81, v81
	v_exp_f32_e32 v82, v82
	v_exp_f32_e32 v83, v83
	v_exp_f32_e32 v84, v84
	v_exp_f32_e32 v85, v85
	s_waitcnt lgkmcnt(2)
	v_mfma_f32_32x32x64_f8f6f4 v[124:139], v[182:189], v[116:123], v[124:139]
	v_exp_f32_e32 v86, v86
	v_exp_f32_e32 v87, v87
	v_exp_f32_e32 v88, v88
	v_exp_f32_e32 v89, v89
	v_exp_f32_e32 v90, v90
	v_exp_f32_e32 v91, v91
	v_exp_f32_e32 v92, v92
	s_waitcnt lgkmcnt(0)
	v_mfma_f32_32x32x64_f8f6f4 v[140:155], v[166:173], v[116:123], v[140:155]
	v_exp_f32_e32 v93, v93
	v_exp_f32_e32 v94, v94
	v_exp_f32_e32 v95, v95
	v_exp_f32_e32 v96, v96
	v_exp_f32_e32 v97, v97
	v_exp_f32_e32 v98, v98
	v_exp_f32_e32 v99, v99
.Lm_m21_end:
	s_sub_i32 s5, s77, 1
	s_cmp_ge_u32 s5, s42
	s_cbranch_scc1 .Lm_t24_end
	v_cvt_pk_fp8_f32 v248, v68, v69
	v_cvt_pk_fp8_f32 v249, v72, v73
	v_cvt_pk_fp8_f32 v250, v76, v77
	v_cvt_pk_fp8_f32 v251, v80, v81
	v_cvt_pk_fp8_f32 v252, v84, v85
	v_cvt_pk_fp8_f32 v253, v88, v89
	v_cvt_pk_fp8_f32 v254, v92, v93
	v_cvt_pk_fp8_f32 v255, v96, v97
	v_cvt_pk_fp8_f32 v248, v70, v71 op_sel:[0,0,1]
	v_cvt_pk_fp8_f32 v249, v74, v75 op_sel:[0,0,1]
	v_cvt_pk_fp8_f32 v250, v78, v79 op_sel:[0,0,1]
	v_cvt_pk_fp8_f32 v251, v82, v83 op_sel:[0,0,1]
	v_cvt_pk_fp8_f32 v252, v86, v87 op_sel:[0,0,1]
	v_cvt_pk_fp8_f32 v253, v90, v91 op_sel:[0,0,1]
	v_cvt_pk_fp8_f32 v254, v94, v95 op_sel:[0,0,1]
	v_cvt_pk_fp8_f32 v255, v98, v99 op_sel:[0,0,1]
	s_nop 1
	v_mfma_f32_32x32x64_f8f6f4 v[68:83], v[218:225], v[248:255], 0

.Lm_nm28:
	ds_read_b128 v[166:169], v207 offset:8192
	ds_read_b128 v[170:173], v208 offset:8192
	ds_read_b128 v[174:177], v207 offset:10240
	ds_read_b128 v[178:181], v208 offset:10240
	ds_read_b128 v[182:185], v207 offset:12288
	ds_read_b128 v[186:189], v208 offset:12288
	s_waitcnt lgkmcnt(4)
	v_mfma_f32_32x32x64_f8f6f4 v[52:67], v[248:255], v[166:173], v[52:67]
	ds_read_b128 v[166:169], v207 offset:14336
	ds_read_b128 v[170:173], v208 offset:14336
	v_max3_f32 v239, v124, v125, v126
	v_max3_f32 v235, v140, v141, v142
	v_max3_f32 v239, v239, v127, v128
	v_max3_f32 v235, v235, v143, v144
	v_max3_f32 v239, v239, v129, v130
	s_waitcnt lgkmcnt(4)
	v_mfma_f32_32x32x64_f8f6f4 v[36:51], v[248:255], v[174:181], v[36:51]
	ds_read_b128 v[174:177], v200 offset:32768
	ds_read_b128 v[178:181], v201 offset:32768
	v_max3_f32 v235, v235, v145, v146
	v_max3_f32 v239, v239, v131, v132
	v_max3_f32 v235, v235, v147, v148
	v_max3_f32 v239, v239, v133, v134
	v_max3_f32 v235, v235, v149, v150
	v_fma_f32 v2, v2, v217, v68
	v_mov_b32_e32 v217, 1.0
	s_waitcnt lgkmcnt(4)
	v_mfma_f32_32x32x64_f8f6f4 v[20:35], v[248:255], v[182:189], v[20:35]
	ds_read_b128 v[182:185], v200 offset:36864
	ds_read_b128 v[186:189], v201 offset:36864
	v_max3_f32 v239, v239, v135, v136
	v_max3_f32 v235, v235, v151, v152
	v_max3_f32 v239, v239, v137, v138
	v_max3_f32 v235, v235, v153, v154
	s_waitcnt lgkmcnt(4)
	v_mfma_f32_32x32x64_f8f6f4 v[4:19], v[248:255], v[166:173], v[4:19]
	ds_read_b128 v[166:169], v202 offset:32768
	ds_read_b128 v[170:173], v203 offset:32768
	v_max3_f32 v239, v239, v139, v155
	v_max_f32_e32 v239, v239, v235
	v_mov_b32_e32 v234, v239
	s_waitcnt lgkmcnt(4)
	v_mfma_f32_32x32x64_f8f6f4 v[68:83], v[174:181], v[100:107], 0
	ds_read_b128 v[174:177], v202 offset:36864
	ds_read_b128 v[178:181], v203 offset:36864
	s_nop 1
	v_permlane32_swap_b32_e32 v239, v234
	v_max_f32_e32 v239, v239, v234
	v_sub_f32_e32 v235, v239, v216
	v_mul_f32_e32 v235, 0x3a93cd3a, v235
	v_cmp_ge_f32_e32 vcc, 2.0, v235
	s_cmp_eq_u64 vcc, exec
	s_cbranch_scc1 .Lm_nr29
	v_max_f32_e32 v235, v216, v239
	v_sub_f32_e32 v217, v216, v235
	v_mul_f32_e32 v217, 0x3ad53b94, v217
	v_exp_f32_e32 v217, v217
	v_mov_b32_e32 v216, v235
	s_and_saveexec_b64 s[6:7], s[0:1]
	ds_write_b32 v214, v217 offset:128
	s_or_b64 exec, exec, s[6:7]
	s_waitcnt lgkmcnt(0)
	ds_read_b128 v[84:87], v213 offset:128
	s_waitcnt lgkmcnt(0)
	v_pk_mul_f32 v[52:53], v[52:53], v[84:85]
	v_pk_mul_f32 v[54:55], v[54:55], v[86:87]
	v_pk_mul_f32 v[36:37], v[36:37], v[84:85]
	v_pk_mul_f32 v[38:39], v[38:39], v[86:87]
	v_pk_mul_f32 v[20:21], v[20:21], v[84:85]
	v_pk_mul_f32 v[22:23], v[22:23], v[86:87]
	v_pk_mul_f32 v[4:5], v[4:5], v[84:85]
	v_pk_mul_f32 v[6:7], v[6:7], v[86:87]
	ds_read_b128 v[84:87], v213 offset:160
	s_waitcnt lgkmcnt(0)
	v_pk_mul_f32 v[56:57], v[56:57], v[84:85]
	v_pk_mul_f32 v[58:59], v[58:59], v[86:87]
	v_pk_mul_f32 v[40:41], v[40:41], v[84:85]
	v_pk_mul_f32 v[42:43], v[42:43], v[86:87]
	v_pk_mul_f32 v[24:25], v[24:25], v[84:85]
	v_pk_mul_f32 v[26:27], v[26:27], v[86:87]
	v_pk_mul_f32 v[8:9], v[8:9], v[84:85]
	v_pk_mul_f32 v[10:11], v[10:11], v[86:87]
	ds_read_b128 v[84:87], v213 offset:192
	s_waitcnt lgkmcnt(0)
	v_pk_mul_f32 v[60:61], v[60:61], v[84:85]
	v_pk_mul_f32 v[62:63], v[62:63], v[86:87]
	v_pk_mul_f32 v[44:45], v[44:45], v[84:85]
	v_pk_mul_f32 v[46:47], v[46:47], v[86:87]
	v_pk_mul_f32 v[28:29], v[28:29], v[84:85]
	v_pk_mul_f32 v[30:31], v[30:31], v[86:87]
	v_pk_mul_f32 v[12:13], v[12:13], v[84:85]
	v_pk_mul_f32 v[14:15], v[14:15], v[86:87]
	ds_read_b128 v[84:87], v213 offset:224
	s_waitcnt lgkmcnt(0)
	v_pk_mul_f32 v[64:65], v[64:65], v[84:85]
	v_pk_mul_f32 v[66:67], v[66:67], v[86:87]
	v_pk_mul_f32 v[48:49], v[48:49], v[84:85]
	v_pk_mul_f32 v[50:51], v[50:51], v[86:87]
	v_pk_mul_f32 v[32:33], v[32:33], v[84:85]
	v_pk_mul_f32 v[34:35], v[34:35], v[86:87]
	v_pk_mul_f32 v[16:17], v[16:17], v[84:85]
	v_pk_mul_f32 v[18:19], v[18:19], v[86:87]
.Lm_nr29:
	v_fmamk_f32 v190, v216, 0xbad53b94, v210
	v_fma_f32 v124, v124, s96, v190
	v_fma_f32 v125, v125, s96, v190
	v_fma_f32 v140, v140, s96, v190
	v_fma_f32 v141, v141, s96, v190
	v_fma_f32 v126, v126, s96, v190
	v_fma_f32 v127, v127, s96, v190
	v_fma_f32 v142, v142, s96, v190
	v_fma_f32 v143, v143, s96, v190
	v_fma_f32 v128, v128, s96, v190
	v_fma_f32 v129, v129, s96, v190
	v_fma_f32 v144, v144, s96, v190
	v_fma_f32 v145, v145, s96, v190
	v_fma_f32 v130, v130, s96, v190
	v_fma_f32 v131, v131, s96, v190
	v_fma_f32 v146, v146, s96, v190
	v_fma_f32 v147, v147, s96, v190
	v_fma_f32 v132, v132, s96, v190
	s_waitcnt lgkmcnt(4)
	v_mfma_f32_32x32x64_f8f6f4 v[84:99], v[182:189], v[100:107], 0
	ds_read_b128 v[182:185], v242 offset:0
	ds_read_b128 v[186:189], v243 offset:0
	v_fma_f32 v133, v133, s96, v190
	v_fma_f32 v148, v148, s96, v190
	v_fma_f32 v149, v149, s96, v190
	v_fma_f32 v134, v134, s96, v190
	v_fma_f32 v135, v135, s96, v190
	v_fma_f32 v150, v150, s96, v190
	v_fma_f32 v151, v151, s96, v190
	v_fma_f32 v136, v136, s96, v190
	v_fma_f32 v137, v137, s96, v190
	v_fma_f32 v152, v152, s96, v190
	v_fma_f32 v153, v153, s96, v190
	v_fma_f32 v138, v138, s96, v190
	v_fma_f32 v139, v139, s96, v190
	v_fma_f32 v154, v154, s96, v190
	v_fma_f32 v155, v155, s96, v190
	v_exp_f32_e32 v124, v124
	v_exp_f32_e32 v125, v125
	v_exp_f32_e32 v126, v126
	s_waitcnt lgkmcnt(4)
	v_mfma_f32_32x32x64_f8f6f4 v[68:83], v[166:173], v[108:115], v[68:83]
	ds_read_b128 v[166:169], v242 offset:4096
	ds_read_b128 v[170:173], v243 offset:4096
	v_exp_f32_e32 v127, v127
	v_exp_f32_e32 v128, v128
	v_exp_f32_e32 v129, v129
	v_exp_f32_e32 v130, v130
	v_exp_f32_e32 v131, v131
	v_exp_f32_e32 v132, v132
	v_exp_f32_e32 v133, v133
	s_waitcnt lgkmcnt(4)
	v_mfma_f32_32x32x64_f8f6f4 v[84:99], v[174:181], v[108:115], v[84:99]
	v_exp_f32_e32 v134, v134
	v_exp_f32_e32 v135, v135
	v_exp_f32_e32 v136, v136
	v_exp_f32_e32 v137, v137
	v_exp_f32_e32 v138, v138
	v_exp_f32_e32 v139, v139
	v_exp_f32_e32 v140, v140
	v_exp_f32_e32 v141, v141
	s_waitcnt lgkmcnt(2)
	v_mfma_f32_32x32x64_f8f6f4 v[68:83], v[182:189], v[116:123], v[68:83]
	v_exp_f32_e32 v142, v142
	v_exp_f32_e32 v143, v143
	v_exp_f32_e32 v144, v144
	v_exp_f32_e32 v145, v145
	v_exp_f32_e32 v146, v146
	v_exp_f32_e32 v147, v147
	v_exp_f32_e32 v148, v148
	s_waitcnt lgkmcnt(0)
	v_mfma_f32_32x32x64_f8f6f4 v[84:99], v[166:173], v[116:123], v[84:99]
	v_exp_f32_e32 v149, v149
	v_exp_f32_e32 v150, v150
	v_exp_f32_e32 v151, v151
	v_exp_f32_e32 v152, v152
	v_exp_f32_e32 v153, v153
	v_exp_f32_e32 v154, v154
	v_exp_f32_e32 v155, v155

.Lm_nm36:
	ds_read_b128 v[166:169], v207 offset:24576
	ds_read_b128 v[170:173], v208 offset:24576
	ds_read_b128 v[174:177], v207 offset:26624
	ds_read_b128 v[178:181], v208 offset:26624
	ds_read_b128 v[182:185], v207 offset:28672
	ds_read_b128 v[186:189], v208 offset:28672
	s_waitcnt lgkmcnt(4)
	v_mfma_f32_32x32x64_f8f6f4 v[52:67], v[248:255], v[166:173], v[52:67]
	ds_read_b128 v[166:169], v207 offset:30720
	ds_read_b128 v[170:173], v208 offset:30720
	v_max3_f32 v239, v68, v69, v70
	v_max3_f32 v235, v84, v85, v86
	v_max3_f32 v239, v239, v71, v72
	v_max3_f32 v235, v235, v87, v88
	v_max3_f32 v239, v239, v73, v74
	s_waitcnt lgkmcnt(4)
	v_mfma_f32_32x32x64_f8f6f4 v[36:51], v[248:255], v[174:181], v[36:51]
	ds_read_b128 v[174:177], v200 offset:49152
	ds_read_b128 v[178:181], v201 offset:49152
	v_max3_f32 v235, v235, v89, v90
	v_max3_f32 v239, v239, v75, v76
	v_max3_f32 v235, v235, v91, v92
	v_max3_f32 v239, v239, v77, v78
	v_max3_f32 v235, v235, v93, v94
	v_fma_f32 v2, v2, v217, v124
	v_mov_b32_e32 v217, 1.0
	s_waitcnt lgkmcnt(4)
	v_mfma_f32_32x32x64_f8f6f4 v[20:35], v[248:255], v[182:189], v[20:35]
	ds_read_b128 v[182:185], v200 offset:53248
	ds_read_b128 v[186:189], v201 offset:53248
	v_max3_f32 v239, v239, v79, v80
	v_max3_f32 v235, v235, v95, v96
	v_max3_f32 v239, v239, v81, v82
	v_max3_f32 v235, v235, v97, v98
	s_waitcnt lgkmcnt(4)
	v_mfma_f32_32x32x64_f8f6f4 v[4:19], v[248:255], v[166:173], v[4:19]
	ds_read_b128 v[166:169], v202 offset:49152
	ds_read_b128 v[170:173], v203 offset:49152
	v_max3_f32 v239, v239, v83, v99
	v_max_f32_e32 v239, v239, v235
	v_mov_b32_e32 v234, v239
	s_waitcnt lgkmcnt(4)
	v_mfma_f32_32x32x64_f8f6f4 v[124:139], v[174:181], v[100:107], 0
	ds_read_b128 v[174:177], v202 offset:53248
	ds_read_b128 v[178:181], v203 offset:53248
	s_nop 1
	v_permlane32_swap_b32_e32 v239, v234
	v_max_f32_e32 v239, v239, v234
	v_sub_f32_e32 v235, v239, v216
	v_mul_f32_e32 v235, 0x3a93cd3a, v235
	v_cmp_ge_f32_e32 vcc, 2.0, v235
	s_cmp_eq_u64 vcc, exec
	s_cbranch_scc1 .Lm_nr37
	v_max_f32_e32 v235, v216, v239
	v_sub_f32_e32 v217, v216, v235
	v_mul_f32_e32 v217, 0x3ad53b94, v217
	v_exp_f32_e32 v217, v217
	v_mov_b32_e32 v216, v235
	s_and_saveexec_b64 s[6:7], s[0:1]
	ds_write_b32 v214, v217 offset:128
	s_or_b64 exec, exec, s[6:7]
	s_waitcnt lgkmcnt(0)
	ds_read_b128 v[140:143], v213 offset:128
	s_waitcnt lgkmcnt(0)
	v_pk_mul_f32 v[52:53], v[52:53], v[140:141]
	v_pk_mul_f32 v[54:55], v[54:55], v[142:143]
	v_pk_mul_f32 v[36:37], v[36:37], v[140:141]
	v_pk_mul_f32 v[38:39], v[38:39], v[142:143]
	v_pk_mul_f32 v[20:21], v[20:21], v[140:141]
	v_pk_mul_f32 v[22:23], v[22:23], v[142:143]
	v_pk_mul_f32 v[4:5], v[4:5], v[140:141]
	v_pk_mul_f32 v[6:7], v[6:7], v[142:143]
	ds_read_b128 v[140:143], v213 offset:160
	s_waitcnt lgkmcnt(0)
	v_pk_mul_f32 v[56:57], v[56:57], v[140:141]
	v_pk_mul_f32 v[58:59], v[58:59], v[142:143]
	v_pk_mul_f32 v[40:41], v[40:41], v[140:141]
	v_pk_mul_f32 v[42:43], v[42:43], v[142:143]
	v_pk_mul_f32 v[24:25], v[24:25], v[140:141]
	v_pk_mul_f32 v[26:27], v[26:27], v[142:143]
	v_pk_mul_f32 v[8:9], v[8:9], v[140:141]
	v_pk_mul_f32 v[10:11], v[10:11], v[142:143]
	ds_read_b128 v[140:143], v213 offset:192
	s_waitcnt lgkmcnt(0)
	v_pk_mul_f32 v[60:61], v[60:61], v[140:141]
	v_pk_mul_f32 v[62:63], v[62:63], v[142:143]
	v_pk_mul_f32 v[44:45], v[44:45], v[140:141]
	v_pk_mul_f32 v[46:47], v[46:47], v[142:143]
	v_pk_mul_f32 v[28:29], v[28:29], v[140:141]
	v_pk_mul_f32 v[30:31], v[30:31], v[142:143]
	v_pk_mul_f32 v[12:13], v[12:13], v[140:141]
	v_pk_mul_f32 v[14:15], v[14:15], v[142:143]
	ds_read_b128 v[140:143], v213 offset:224
	s_waitcnt lgkmcnt(0)
	v_pk_mul_f32 v[64:65], v[64:65], v[140:141]
	v_pk_mul_f32 v[66:67], v[66:67], v[142:143]
	v_pk_mul_f32 v[48:49], v[48:49], v[140:141]
	v_pk_mul_f32 v[50:51], v[50:51], v[142:143]
	v_pk_mul_f32 v[32:33], v[32:33], v[140:141]
	v_pk_mul_f32 v[34:35], v[34:35], v[142:143]
	v_pk_mul_f32 v[16:17], v[16:17], v[140:141]
	v_pk_mul_f32 v[18:19], v[18:19], v[142:143]
.Lm_nr37:
	v_fmamk_f32 v190, v216, 0xbad53b94, v210
	v_fma_f32 v68, v68, s96, v190
	v_fma_f32 v69, v69, s96, v190
	v_fma_f32 v84, v84, s96, v190
	v_fma_f32 v85, v85, s96, v190
	v_fma_f32 v70, v70, s96, v190
	v_fma_f32 v71, v71, s96, v190
	v_fma_f32 v86, v86, s96, v190
	v_fma_f32 v87, v87, s96, v190
	v_fma_f32 v72, v72, s96, v190
	v_fma_f32 v73, v73, s96, v190
	v_fma_f32 v88, v88, s96, v190
	v_fma_f32 v89, v89, s96, v190
	v_fma_f32 v74, v74, s96, v190
	v_fma_f32 v75, v75, s96, v190
	v_fma_f32 v90, v90, s96, v190
	v_fma_f32 v91, v91, s96, v190
	v_fma_f32 v76, v76, s96, v190
	s_waitcnt lgkmcnt(4)
	v_mfma_f32_32x32x64_f8f6f4 v[140:155], v[182:189], v[100:107], 0
	ds_read_b128 v[182:185], v242 offset:8192
	ds_read_b128 v[186:189], v243 offset:8192
	v_fma_f32 v77, v77, s96, v190
	v_fma_f32 v92, v92, s96, v190
	v_fma_f32 v93, v93, s96, v190
	v_fma_f32 v78, v78, s96, v190
	v_fma_f32 v79, v79, s96, v190
	v_fma_f32 v94, v94, s96, v190
	v_fma_f32 v95, v95, s96, v190
	v_fma_f32 v80, v80, s96, v190
	v_fma_f32 v81, v81, s96, v190
	v_fma_f32 v96, v96, s96, v190
	v_fma_f32 v97, v97, s96, v190
	v_fma_f32 v82, v82, s96, v190
	v_fma_f32 v83, v83, s96, v190
	v_fma_f32 v98, v98, s96, v190
	v_fma_f32 v99, v99, s96, v190
	v_exp_f32_e32 v68, v68
	v_exp_f32_e32 v69, v69
	v_exp_f32_e32 v70, v70
	s_waitcnt lgkmcnt(4)
	v_mfma_f32_32x32x64_f8f6f4 v[124:139], v[166:173], v[108:115], v[124:139]
	ds_read_b128 v[166:169], v242 offset:12288
	ds_read_b128 v[170:173], v243 offset:12288
	v_exp_f32_e32 v71, v71
	v_exp_f32_e32 v72, v72
	v_exp_f32_e32 v73, v73
	v_exp_f32_e32 v74, v74
	v_exp_f32_e32 v75, v75
	v_exp_f32_e32 v76, v76
	v_exp_f32_e32 v77, v77
	s_waitcnt lgkmcnt(4)
	v_mfma_f32_32x32x64_f8f6f4 v[140:155], v[174:181], v[108:115], v[140:155]
	v_exp_f32_e32 v78, v78
	v_exp_f32_e32 v79, v79
	v_exp_f32_e32 v80, v80
	v_exp_f32_e32 v81, v81
	v_exp_f32_e32 v82, v82
	v_exp_f32_e32 v83, v83
	v_exp_f32_e32 v84, v84
	v_exp_f32_e32 v85, v85
	s_waitcnt lgkmcnt(2)
	v_mfma_f32_32x32x64_f8f6f4 v[124:139], v[182:189], v[116:123], v[124:139]
	v_exp_f32_e32 v86, v86
	v_exp_f32_e32 v87, v87
	v_exp_f32_e32 v88, v88
	v_exp_f32_e32 v89, v89
	v_exp_f32_e32 v90, v90
	v_exp_f32_e32 v91, v91
	v_exp_f32_e32 v92, v92
	s_waitcnt lgkmcnt(0)
	v_mfma_f32_32x32x64_f8f6f4 v[140:155], v[166:173], v[116:123], v[140:155]
	v_exp_f32_e32 v93, v93
	v_exp_f32_e32 v94, v94
	v_exp_f32_e32 v95, v95
	v_exp_f32_e32 v96, v96
	v_exp_f32_e32 v97, v97
	v_exp_f32_e32 v98, v98
	v_exp_f32_e32 v99, v99

.Lm_nd59:
	s_sub_i32 s5, s77, 2
	s_cmp_ge_u32 s5, s42
	s_cbranch_scc1 .Lm_t60_end
	v_cvt_pk_fp8_f32 v248, v68, v69
	v_cvt_pk_fp8_f32 v249, v72, v73
	v_cvt_pk_fp8_f32 v250, v76, v77
	v_cvt_pk_fp8_f32 v251, v80, v81
	v_cvt_pk_fp8_f32 v252, v84, v85
	v_cvt_pk_fp8_f32 v253, v88, v89
	v_cvt_pk_fp8_f32 v254, v92, v93
	v_cvt_pk_fp8_f32 v255, v96, v97
	v_cvt_pk_fp8_f32 v248, v70, v71 op_sel:[0,0,1]
	v_cvt_pk_fp8_f32 v249, v74, v75 op_sel:[0,0,1]
	v_cvt_pk_fp8_f32 v250, v78, v79 op_sel:[0,0,1]
	v_cvt_pk_fp8_f32 v251, v82, v83 op_sel:[0,0,1]
	v_cvt_pk_fp8_f32 v252, v86, v87 op_sel:[0,0,1]
	v_cvt_pk_fp8_f32 v253, v90, v91 op_sel:[0,0,1]
	v_cvt_pk_fp8_f32 v254, v94, v95 op_sel:[0,0,1]
	v_cvt_pk_fp8_f32 v255, v98, v99 op_sel:[0,0,1]
	s_nop 1
	v_mfma_f32_32x32x64_f8f6f4 v[68:83], v[218:225], v[248:255], 0

.Lm_nd67:
	s_sub_i32 s5, s77, 2
	s_cmp_ge_u32 s5, s42
	s_cbranch_scc1 .Lm_t68_end
	v_cvt_pk_fp8_f32 v248, v124, v125
	v_cvt_pk_fp8_f32 v249, v128, v129
	v_cvt_pk_fp8_f32 v250, v132, v133
	v_cvt_pk_fp8_f32 v251, v136, v137
	v_cvt_pk_fp8_f32 v252, v140, v141
	v_cvt_pk_fp8_f32 v253, v144, v145
	v_cvt_pk_fp8_f32 v254, v148, v149
	v_cvt_pk_fp8_f32 v255, v152, v153
	v_cvt_pk_fp8_f32 v248, v126, v127 op_sel:[0,0,1]
	v_cvt_pk_fp8_f32 v249, v130, v131 op_sel:[0,0,1]
	v_cvt_pk_fp8_f32 v250, v134, v135 op_sel:[0,0,1]
	v_cvt_pk_fp8_f32 v251, v138, v139 op_sel:[0,0,1]
	v_cvt_pk_fp8_f32 v252, v142, v143 op_sel:[0,0,1]
	v_cvt_pk_fp8_f32 v253, v146, v147 op_sel:[0,0,1]
	v_cvt_pk_fp8_f32 v254, v150, v151 op_sel:[0,0,1]
	v_cvt_pk_fp8_f32 v255, v154, v155 op_sel:[0,0,1]
	s_nop 1
	v_mfma_f32_32x32x64_f8f6f4 v[124:139], v[218:225], v[248:255], 0

.Lm_m88_end:
	s_add_i32 s77, s77, 1
	v_subrev_u32_e32 v215, 64, v215
	s_sub_i32 s5, s77, 2
	s_cmp_ge_u32 s5, s42
	s_cbranch_scc1 .Lm_t91_end
	v_cvt_pk_fp8_f32 v248, v124, v125
	v_cvt_pk_fp8_f32 v249, v128, v129
	v_cvt_pk_fp8_f32 v250, v132, v133
	v_cvt_pk_fp8_f32 v251, v136, v137
	v_cvt_pk_fp8_f32 v252, v140, v141
	v_cvt_pk_fp8_f32 v253, v144, v145
	v_cvt_pk_fp8_f32 v254, v148, v149
	v_cvt_pk_fp8_f32 v255, v152, v153
	v_cvt_pk_fp8_f32 v248, v126, v127 op_sel:[0,0,1]
	v_cvt_pk_fp8_f32 v249, v130, v131 op_sel:[0,0,1]
	v_cvt_pk_fp8_f32 v250, v134, v135 op_sel:[0,0,1]
	v_cvt_pk_fp8_f32 v251, v138, v139 op_sel:[0,0,1]
	v_cvt_pk_fp8_f32 v252, v142, v143 op_sel:[0,0,1]
	v_cvt_pk_fp8_f32 v253, v146, v147 op_sel:[0,0,1]
	v_cvt_pk_fp8_f32 v254, v150, v151 op_sel:[0,0,1]
	v_cvt_pk_fp8_f32 v255, v154, v155 op_sel:[0,0,1]
	s_nop 1
	v_mfma_f32_32x32x64_f8f6f4 v[124:139], v[218:225], v[248:255], 0

.Lm_nm96:
	ds_read_b128 v[166:169], v207 offset:0
	ds_read_b128 v[170:173], v208 offset:0
	ds_read_b128 v[174:177], v207 offset:2048
	ds_read_b128 v[178:181], v208 offset:2048
	ds_read_b128 v[182:185], v207 offset:4096
	ds_read_b128 v[186:189], v208 offset:4096
	s_waitcnt lgkmcnt(4)
	v_mfma_f32_32x32x64_f8f6f4 v[52:67], v[248:255], v[166:173], v[52:67]
	ds_read_b128 v[166:169], v207 offset:6144
	ds_read_b128 v[170:173], v208 offset:6144
	s_waitcnt lgkmcnt(4)
	v_mfma_f32_32x32x64_f8f6f4 v[36:51], v[248:255], v[174:181], v[36:51]
	s_waitcnt lgkmcnt(2)
	v_mfma_f32_32x32x64_f8f6f4 v[20:35], v[248:255], v[182:189], v[20:35]
	s_waitcnt lgkmcnt(0)
	v_mfma_f32_32x32x64_f8f6f4 v[4:19], v[248:255], v[166:173], v[4:19]
	s_nop 7
	v_fma_f32 v2, v2, v217, v68
	v_mov_b32_e32 v217, 1.0
	v_max3_f32 v239, v124, v125, v126
	v_max3_f32 v235, v140, v141, v142
	v_max3_f32 v239, v239, v127, v128
	v_max3_f32 v235, v235, v143, v144
	v_max3_f32 v239, v239, v129, v130
	v_max3_f32 v235, v235, v145, v146
	v_max3_f32 v239, v239, v131, v132
	v_max3_f32 v235, v235, v147, v148
	v_max3_f32 v239, v239, v133, v134
	v_max3_f32 v235, v235, v149, v150
	v_max3_f32 v239, v239, v135, v136
	v_max3_f32 v235, v235, v151, v152
	v_max3_f32 v239, v239, v137, v138
	v_max3_f32 v235, v235, v153, v154
	v_max3_f32 v239, v239, v139, v155
	v_max_f32_e32 v239, v239, v235
	v_mov_b32_e32 v234, v239
	s_nop 1
	v_permlane32_swap_b32_e32 v239, v234
	v_max_f32_e32 v239, v239, v234
	v_sub_f32_e32 v235, v239, v216
	v_mul_f32_e32 v235, 0x3a93cd3a, v235
	v_cmp_ge_f32_e32 vcc, 2.0, v235
	s_cmp_eq_u64 vcc, exec
	s_cbranch_scc1 .Lm_nr97
	v_max_f32_e32 v235, v216, v239
	v_sub_f32_e32 v217, v216, v235
	v_mul_f32_e32 v217, 0x3ad53b94, v217
	v_exp_f32_e32 v217, v217
	v_mov_b32_e32 v216, v235
	s_and_saveexec_b64 s[6:7], s[0:1]
	ds_write_b32 v214, v217 offset:128
	s_or_b64 exec, exec, s[6:7]
	s_waitcnt lgkmcnt(0)
	ds_read_b128 v[84:87], v213 offset:128
	s_waitcnt lgkmcnt(0)
	v_pk_mul_f32 v[52:53], v[52:53], v[84:85]
	v_pk_mul_f32 v[54:55], v[54:55], v[86:87]
	v_pk_mul_f32 v[36:37], v[36:37], v[84:85]
	v_pk_mul_f32 v[38:39], v[38:39], v[86:87]
	v_pk_mul_f32 v[20:21], v[20:21], v[84:85]
	v_pk_mul_f32 v[22:23], v[22:23], v[86:87]
	v_pk_mul_f32 v[4:5], v[4:5], v[84:85]
	v_pk_mul_f32 v[6:7], v[6:7], v[86:87]
	ds_read_b128 v[84:87], v213 offset:160
	s_waitcnt lgkmcnt(0)
	v_pk_mul_f32 v[56:57], v[56:57], v[84:85]
	v_pk_mul_f32 v[58:59], v[58:59], v[86:87]
	v_pk_mul_f32 v[40:41], v[40:41], v[84:85]
	v_pk_mul_f32 v[42:43], v[42:43], v[86:87]
	v_pk_mul_f32 v[24:25], v[24:25], v[84:85]
	v_pk_mul_f32 v[26:27], v[26:27], v[86:87]
	v_pk_mul_f32 v[8:9], v[8:9], v[84:85]
	v_pk_mul_f32 v[10:11], v[10:11], v[86:87]
	ds_read_b128 v[84:87], v213 offset:192
	s_waitcnt lgkmcnt(0)
	v_pk_mul_f32 v[60:61], v[60:61], v[84:85]
	v_pk_mul_f32 v[62:63], v[62:63], v[86:87]
	v_pk_mul_f32 v[44:45], v[44:45], v[84:85]
	v_pk_mul_f32 v[46:47], v[46:47], v[86:87]
	v_pk_mul_f32 v[28:29], v[28:29], v[84:85]
	v_pk_mul_f32 v[30:31], v[30:31], v[86:87]
	v_pk_mul_f32 v[12:13], v[12:13], v[84:85]
	v_pk_mul_f32 v[14:15], v[14:15], v[86:87]
	ds_read_b128 v[84:87], v213 offset:224
	s_waitcnt lgkmcnt(0)
	v_pk_mul_f32 v[64:65], v[64:65], v[84:85]
	v_pk_mul_f32 v[66:67], v[66:67], v[86:87]
	v_pk_mul_f32 v[48:49], v[48:49], v[84:85]
	v_pk_mul_f32 v[50:51], v[50:51], v[86:87]
	v_pk_mul_f32 v[32:33], v[32:33], v[84:85]
	v_pk_mul_f32 v[34:35], v[34:35], v[86:87]
	v_pk_mul_f32 v[16:17], v[16:17], v[84:85]
	v_pk_mul_f32 v[18:19], v[18:19], v[86:87]

.Lm_m13_s2:
	s_sub_i32 s5, s77, 1
	s_cmp_lg_u32 s5, s42
	s_cbranch_scc1 .Lm_m13_end
	ds_read_b128 v[166:169], v207 offset:0
	ds_read_b128 v[170:173], v208 offset:0
	ds_read_b128 v[174:177], v207 offset:2048
	ds_read_b128 v[178:181], v208 offset:2048
	ds_read_b128 v[182:185], v207 offset:4096
	ds_read_b128 v[186:189], v208 offset:4096
	s_waitcnt lgkmcnt(4)
	v_mfma_f32_32x32x64_f8f6f4 v[52:67], v[248:255], v[166:173], v[52:67]
	ds_read_b128 v[166:169], v207 offset:6144
	ds_read_b128 v[170:173], v208 offset:6144
	s_waitcnt lgkmcnt(4)
	v_mfma_f32_32x32x64_f8f6f4 v[36:51], v[248:255], v[174:181], v[36:51]
	s_waitcnt lgkmcnt(2)
	v_mfma_f32_32x32x64_f8f6f4 v[20:35], v[248:255], v[182:189], v[20:35]
	s_waitcnt lgkmcnt(0)
	v_mfma_f32_32x32x64_f8f6f4 v[4:19], v[248:255], v[166:173], v[4:19]
	s_nop 7
	v_fma_f32 v2, v2, v217, v68
	v_mov_b32_e32 v217, 1.0
	s_branch .Lm_m13_end

.Lm_nm98:
	ds_read_b128 v[166:169], v207 offset:16384
	ds_read_b128 v[170:173], v208 offset:16384
	ds_read_b128 v[174:177], v207 offset:18432
	ds_read_b128 v[178:181], v208 offset:18432
	ds_read_b128 v[182:185], v207 offset:20480
	ds_read_b128 v[186:189], v208 offset:20480
	s_waitcnt lgkmcnt(4)
	v_mfma_f32_32x32x64_f8f6f4 v[52:67], v[248:255], v[166:173], v[52:67]
	ds_read_b128 v[166:169], v207 offset:22528
	ds_read_b128 v[170:173], v208 offset:22528
	s_waitcnt lgkmcnt(4)
	v_mfma_f32_32x32x64_f8f6f4 v[36:51], v[248:255], v[174:181], v[36:51]
	s_waitcnt lgkmcnt(2)
	v_mfma_f32_32x32x64_f8f6f4 v[20:35], v[248:255], v[182:189], v[20:35]
	s_waitcnt lgkmcnt(0)
	v_mfma_f32_32x32x64_f8f6f4 v[4:19], v[248:255], v[166:173], v[4:19]
	s_nop 7
	v_fma_f32 v2, v2, v217, v124
	v_mov_b32_e32 v217, 1.0
	v_max3_f32 v239, v68, v69, v70
	v_max3_f32 v235, v84, v85, v86
	v_max3_f32 v239, v239, v71, v72
	v_max3_f32 v235, v235, v87, v88
	v_max3_f32 v239, v239, v73, v74
	v_max3_f32 v235, v235, v89, v90
	v_max3_f32 v239, v239, v75, v76
	v_max3_f32 v235, v235, v91, v92
	v_max3_f32 v239, v239, v77, v78
	v_max3_f32 v235, v235, v93, v94
	v_max3_f32 v239, v239, v79, v80
	v_max3_f32 v235, v235, v95, v96
	v_max3_f32 v239, v239, v81, v82
	v_max3_f32 v235, v235, v97, v98
	v_max3_f32 v239, v239, v83, v99
	v_max_f32_e32 v239, v239, v235
	v_mov_b32_e32 v234, v239
	s_nop 1
	v_permlane32_swap_b32_e32 v239, v234
	v_max_f32_e32 v239, v239, v234
	v_sub_f32_e32 v235, v239, v216
	v_mul_f32_e32 v235, 0x3a93cd3a, v235
	v_cmp_ge_f32_e32 vcc, 2.0, v235
	s_cmp_eq_u64 vcc, exec
	s_cbranch_scc1 .Lm_nr99
	v_max_f32_e32 v235, v216, v239
	v_sub_f32_e32 v217, v216, v235
	v_mul_f32_e32 v217, 0x3ad53b94, v217
	v_exp_f32_e32 v217, v217
	v_mov_b32_e32 v216, v235
	s_and_saveexec_b64 s[6:7], s[0:1]
	ds_write_b32 v214, v217 offset:128
	s_or_b64 exec, exec, s[6:7]
	s_waitcnt lgkmcnt(0)
	ds_read_b128 v[140:143], v213 offset:128
	s_waitcnt lgkmcnt(0)
	v_pk_mul_f32 v[52:53], v[52:53], v[140:141]
	v_pk_mul_f32 v[54:55], v[54:55], v[142:143]
	v_pk_mul_f32 v[36:37], v[36:37], v[140:141]
	v_pk_mul_f32 v[38:39], v[38:39], v[142:143]
	v_pk_mul_f32 v[20:21], v[20:21], v[140:141]
	v_pk_mul_f32 v[22:23], v[22:23], v[142:143]
	v_pk_mul_f32 v[4:5], v[4:5], v[140:141]
	v_pk_mul_f32 v[6:7], v[6:7], v[142:143]
	ds_read_b128 v[140:143], v213 offset:160
	s_waitcnt lgkmcnt(0)
	v_pk_mul_f32 v[56:57], v[56:57], v[140:141]
	v_pk_mul_f32 v[58:59], v[58:59], v[142:143]
	v_pk_mul_f32 v[40:41], v[40:41], v[140:141]
	v_pk_mul_f32 v[42:43], v[42:43], v[142:143]
	v_pk_mul_f32 v[24:25], v[24:25], v[140:141]
	v_pk_mul_f32 v[26:27], v[26:27], v[142:143]
	v_pk_mul_f32 v[8:9], v[8:9], v[140:141]
	v_pk_mul_f32 v[10:11], v[10:11], v[142:143]
	ds_read_b128 v[140:143], v213 offset:192
	s_waitcnt lgkmcnt(0)
	v_pk_mul_f32 v[60:61], v[60:61], v[140:141]
	v_pk_mul_f32 v[62:63], v[62:63], v[142:143]
	v_pk_mul_f32 v[44:45], v[44:45], v[140:141]
	v_pk_mul_f32 v[46:47], v[46:47], v[142:143]
	v_pk_mul_f32 v[28:29], v[28:29], v[140:141]
	v_pk_mul_f32 v[30:31], v[30:31], v[142:143]
	v_pk_mul_f32 v[12:13], v[12:13], v[140:141]
	v_pk_mul_f32 v[14:15], v[14:15], v[142:143]
	ds_read_b128 v[140:143], v213 offset:224
	s_waitcnt lgkmcnt(0)
	v_pk_mul_f32 v[64:65], v[64:65], v[140:141]
	v_pk_mul_f32 v[66:67], v[66:67], v[142:143]
	v_pk_mul_f32 v[48:49], v[48:49], v[140:141]
	v_pk_mul_f32 v[50:51], v[50:51], v[142:143]
	v_pk_mul_f32 v[32:33], v[32:33], v[140:141]
	v_pk_mul_f32 v[34:35], v[34:35], v[142:143]
	v_pk_mul_f32 v[16:17], v[16:17], v[140:141]
	v_pk_mul_f32 v[18:19], v[18:19], v[142:143]

.Lm_m21_s2:
	s_sub_i32 s5, s77, 1
	s_cmp_lg_u32 s5, s42
	s_cbranch_scc1 .Lm_m21_end
	ds_read_b128 v[166:169], v207 offset:16384
	ds_read_b128 v[170:173], v208 offset:16384
	ds_read_b128 v[174:177], v207 offset:18432
	ds_read_b128 v[178:181], v208 offset:18432
	ds_read_b128 v[182:185], v207 offset:20480
	ds_read_b128 v[186:189], v208 offset:20480
	s_waitcnt lgkmcnt(4)
	v_mfma_f32_32x32x64_f8f6f4 v[52:67], v[248:255], v[166:173], v[52:67]
	ds_read_b128 v[166:169], v207 offset:22528
	ds_read_b128 v[170:173], v208 offset:22528
	s_waitcnt lgkmcnt(4)
	v_mfma_f32_32x32x64_f8f6f4 v[36:51], v[248:255], v[174:181], v[36:51]
	s_waitcnt lgkmcnt(2)
	v_mfma_f32_32x32x64_f8f6f4 v[20:35], v[248:255], v[182:189], v[20:35]
	s_waitcnt lgkmcnt(0)
	v_mfma_f32_32x32x64_f8f6f4 v[4:19], v[248:255], v[166:173], v[4:19]
	s_nop 7
	v_fma_f32 v2, v2, v217, v124
	v_mov_b32_e32 v217, 1.0
	s_branch .Lm_m21_end

.Lm_nm100:
	ds_read_b128 v[166:169], v207 offset:8192
	ds_read_b128 v[170:173], v208 offset:8192
	ds_read_b128 v[174:177], v207 offset:10240
	ds_read_b128 v[178:181], v208 offset:10240
	ds_read_b128 v[182:185], v207 offset:12288
	ds_read_b128 v[186:189], v208 offset:12288
	s_waitcnt lgkmcnt(4)
	v_mfma_f32_32x32x64_f8f6f4 v[52:67], v[248:255], v[166:173], v[52:67]
	ds_read_b128 v[166:169], v207 offset:14336
	ds_read_b128 v[170:173], v208 offset:14336
	s_waitcnt lgkmcnt(4)
	v_mfma_f32_32x32x64_f8f6f4 v[36:51], v[248:255], v[174:181], v[36:51]
	s_waitcnt lgkmcnt(2)
	v_mfma_f32_32x32x64_f8f6f4 v[20:35], v[248:255], v[182:189], v[20:35]
	s_waitcnt lgkmcnt(0)
	v_mfma_f32_32x32x64_f8f6f4 v[4:19], v[248:255], v[166:173], v[4:19]
	s_nop 7
	v_fma_f32 v2, v2, v217, v68
	v_mov_b32_e32 v217, 1.0
	v_max3_f32 v239, v124, v125, v126
	v_max3_f32 v235, v140, v141, v142
	v_max3_f32 v239, v239, v127, v128
	v_max3_f32 v235, v235, v143, v144
	v_max3_f32 v239, v239, v129, v130
	v_max3_f32 v235, v235, v145, v146
	v_max3_f32 v239, v239, v131, v132
	v_max3_f32 v235, v235, v147, v148
	v_max3_f32 v239, v239, v133, v134
	v_max3_f32 v235, v235, v149, v150
	v_max3_f32 v239, v239, v135, v136
	v_max3_f32 v235, v235, v151, v152
	v_max3_f32 v239, v239, v137, v138
	v_max3_f32 v235, v235, v153, v154
	v_max3_f32 v239, v239, v139, v155
	v_max_f32_e32 v239, v239, v235
	v_mov_b32_e32 v234, v239
	s_nop 1
	v_permlane32_swap_b32_e32 v239, v234
	v_max_f32_e32 v239, v239, v234
	v_sub_f32_e32 v235, v239, v216
	v_mul_f32_e32 v235, 0x3a93cd3a, v235
	v_cmp_ge_f32_e32 vcc, 2.0, v235
	s_cmp_eq_u64 vcc, exec
	s_cbranch_scc1 .Lm_nr101
	v_max_f32_e32 v235, v216, v239
	v_sub_f32_e32 v217, v216, v235
	v_mul_f32_e32 v217, 0x3ad53b94, v217
	v_exp_f32_e32 v217, v217
	v_mov_b32_e32 v216, v235
	s_and_saveexec_b64 s[6:7], s[0:1]
	ds_write_b32 v214, v217 offset:128
	s_or_b64 exec, exec, s[6:7]
	s_waitcnt lgkmcnt(0)
	ds_read_b128 v[84:87], v213 offset:128
	s_waitcnt lgkmcnt(0)
	v_pk_mul_f32 v[52:53], v[52:53], v[84:85]
	v_pk_mul_f32 v[54:55], v[54:55], v[86:87]
	v_pk_mul_f32 v[36:37], v[36:37], v[84:85]
	v_pk_mul_f32 v[38:39], v[38:39], v[86:87]
	v_pk_mul_f32 v[20:21], v[20:21], v[84:85]
	v_pk_mul_f32 v[22:23], v[22:23], v[86:87]
	v_pk_mul_f32 v[4:5], v[4:5], v[84:85]
	v_pk_mul_f32 v[6:7], v[6:7], v[86:87]
	ds_read_b128 v[84:87], v213 offset:160
	s_waitcnt lgkmcnt(0)
	v_pk_mul_f32 v[56:57], v[56:57], v[84:85]
	v_pk_mul_f32 v[58:59], v[58:59], v[86:87]
	v_pk_mul_f32 v[40:41], v[40:41], v[84:85]
	v_pk_mul_f32 v[42:43], v[42:43], v[86:87]
	v_pk_mul_f32 v[24:25], v[24:25], v[84:85]
	v_pk_mul_f32 v[26:27], v[26:27], v[86:87]
	v_pk_mul_f32 v[8:9], v[8:9], v[84:85]
	v_pk_mul_f32 v[10:11], v[10:11], v[86:87]
	ds_read_b128 v[84:87], v213 offset:192
	s_waitcnt lgkmcnt(0)
	v_pk_mul_f32 v[60:61], v[60:61], v[84:85]
	v_pk_mul_f32 v[62:63], v[62:63], v[86:87]
	v_pk_mul_f32 v[44:45], v[44:45], v[84:85]
	v_pk_mul_f32 v[46:47], v[46:47], v[86:87]
	v_pk_mul_f32 v[28:29], v[28:29], v[84:85]
	v_pk_mul_f32 v[30:31], v[30:31], v[86:87]
	v_pk_mul_f32 v[12:13], v[12:13], v[84:85]
	v_pk_mul_f32 v[14:15], v[14:15], v[86:87]
	ds_read_b128 v[84:87], v213 offset:224
	s_waitcnt lgkmcnt(0)
	v_pk_mul_f32 v[64:65], v[64:65], v[84:85]
	v_pk_mul_f32 v[66:67], v[66:67], v[86:87]
	v_pk_mul_f32 v[48:49], v[48:49], v[84:85]
	v_pk_mul_f32 v[50:51], v[50:51], v[86:87]
	v_pk_mul_f32 v[32:33], v[32:33], v[84:85]
	v_pk_mul_f32 v[34:35], v[34:35], v[86:87]
	v_pk_mul_f32 v[16:17], v[16:17], v[84:85]
	v_pk_mul_f32 v[18:19], v[18:19], v[86:87]

.Lm_m27_s2:
	s_sub_i32 s5, s77, 1
	s_cmp_lg_u32 s5, s42
	s_cbranch_scc1 .Lm_m27_end
	ds_read_b128 v[166:169], v207 offset:8192
	ds_read_b128 v[170:173], v208 offset:8192
	ds_read_b128 v[174:177], v207 offset:10240
	ds_read_b128 v[178:181], v208 offset:10240
	ds_read_b128 v[182:185], v207 offset:12288
	ds_read_b128 v[186:189], v208 offset:12288
	s_waitcnt lgkmcnt(4)
	v_mfma_f32_32x32x64_f8f6f4 v[52:67], v[248:255], v[166:173], v[52:67]
	ds_read_b128 v[166:169], v207 offset:14336
	ds_read_b128 v[170:173], v208 offset:14336
	s_waitcnt lgkmcnt(4)
	v_mfma_f32_32x32x64_f8f6f4 v[36:51], v[248:255], v[174:181], v[36:51]
	s_waitcnt lgkmcnt(2)
	v_mfma_f32_32x32x64_f8f6f4 v[20:35], v[248:255], v[182:189], v[20:35]
	s_waitcnt lgkmcnt(0)
	v_mfma_f32_32x32x64_f8f6f4 v[4:19], v[248:255], v[166:173], v[4:19]
	s_nop 7
	v_fma_f32 v2, v2, v217, v68
	v_mov_b32_e32 v217, 1.0
	s_branch .Lm_m27_end

.Lm_nm102:
	ds_read_b128 v[166:169], v207 offset:24576
	ds_read_b128 v[170:173], v208 offset:24576
	ds_read_b128 v[174:177], v207 offset:26624
	ds_read_b128 v[178:181], v208 offset:26624
	ds_read_b128 v[182:185], v207 offset:28672
	ds_read_b128 v[186:189], v208 offset:28672
	s_waitcnt lgkmcnt(4)
	v_mfma_f32_32x32x64_f8f6f4 v[52:67], v[248:255], v[166:173], v[52:67]
	ds_read_b128 v[166:169], v207 offset:30720
	ds_read_b128 v[170:173], v208 offset:30720
	s_waitcnt lgkmcnt(4)
	v_mfma_f32_32x32x64_f8f6f4 v[36:51], v[248:255], v[174:181], v[36:51]
	s_waitcnt lgkmcnt(2)
	v_mfma_f32_32x32x64_f8f6f4 v[20:35], v[248:255], v[182:189], v[20:35]
	s_waitcnt lgkmcnt(0)
	v_mfma_f32_32x32x64_f8f6f4 v[4:19], v[248:255], v[166:173], v[4:19]
	s_nop 7
	v_fma_f32 v2, v2, v217, v124
	v_mov_b32_e32 v217, 1.0
	v_max3_f32 v239, v68, v69, v70
	v_max3_f32 v235, v84, v85, v86
	v_max3_f32 v239, v239, v71, v72
	v_max3_f32 v235, v235, v87, v88
	v_max3_f32 v239, v239, v73, v74
	v_max3_f32 v235, v235, v89, v90
	v_max3_f32 v239, v239, v75, v76
	v_max3_f32 v235, v235, v91, v92
	v_max3_f32 v239, v239, v77, v78
	v_max3_f32 v235, v235, v93, v94
	v_max3_f32 v239, v239, v79, v80
	v_max3_f32 v235, v235, v95, v96
	v_max3_f32 v239, v239, v81, v82
	v_max3_f32 v235, v235, v97, v98
	v_max3_f32 v239, v239, v83, v99
	v_max_f32_e32 v239, v239, v235
	v_mov_b32_e32 v234, v239
	s_nop 1
	v_permlane32_swap_b32_e32 v239, v234
	v_max_f32_e32 v239, v239, v234
	v_sub_f32_e32 v235, v239, v216
	v_mul_f32_e32 v235, 0x3a93cd3a, v235
	v_cmp_ge_f32_e32 vcc, 2.0, v235
	s_cmp_eq_u64 vcc, exec
	s_cbranch_scc1 .Lm_nr103
	v_max_f32_e32 v235, v216, v239
	v_sub_f32_e32 v217, v216, v235
	v_mul_f32_e32 v217, 0x3ad53b94, v217
	v_exp_f32_e32 v217, v217
	v_mov_b32_e32 v216, v235
	s_and_saveexec_b64 s[6:7], s[0:1]
	ds_write_b32 v214, v217 offset:128
	s_or_b64 exec, exec, s[6:7]
	s_waitcnt lgkmcnt(0)
	ds_read_b128 v[140:143], v213 offset:128
	s_waitcnt lgkmcnt(0)
	v_pk_mul_f32 v[52:53], v[52:53], v[140:141]
	v_pk_mul_f32 v[54:55], v[54:55], v[142:143]
	v_pk_mul_f32 v[36:37], v[36:37], v[140:141]
	v_pk_mul_f32 v[38:39], v[38:39], v[142:143]
	v_pk_mul_f32 v[20:21], v[20:21], v[140:141]
	v_pk_mul_f32 v[22:23], v[22:23], v[142:143]
	v_pk_mul_f32 v[4:5], v[4:5], v[140:141]
	v_pk_mul_f32 v[6:7], v[6:7], v[142:143]
	ds_read_b128 v[140:143], v213 offset:160
	s_waitcnt lgkmcnt(0)
	v_pk_mul_f32 v[56:57], v[56:57], v[140:141]
	v_pk_mul_f32 v[58:59], v[58:59], v[142:143]
	v_pk_mul_f32 v[40:41], v[40:41], v[140:141]
	v_pk_mul_f32 v[42:43], v[42:43], v[142:143]
	v_pk_mul_f32 v[24:25], v[24:25], v[140:141]
	v_pk_mul_f32 v[26:27], v[26:27], v[142:143]
	v_pk_mul_f32 v[8:9], v[8:9], v[140:141]
	v_pk_mul_f32 v[10:11], v[10:11], v[142:143]
	ds_read_b128 v[140:143], v213 offset:192
	s_waitcnt lgkmcnt(0)
	v_pk_mul_f32 v[60:61], v[60:61], v[140:141]
	v_pk_mul_f32 v[62:63], v[62:63], v[142:143]
	v_pk_mul_f32 v[44:45], v[44:45], v[140:141]
	v_pk_mul_f32 v[46:47], v[46:47], v[142:143]
	v_pk_mul_f32 v[28:29], v[28:29], v[140:141]
	v_pk_mul_f32 v[30:31], v[30:31], v[142:143]
	v_pk_mul_f32 v[12:13], v[12:13], v[140:141]
	v_pk_mul_f32 v[14:15], v[14:15], v[142:143]
	ds_read_b128 v[140:143], v213 offset:224
	s_waitcnt lgkmcnt(0)
	v_pk_mul_f32 v[64:65], v[64:65], v[140:141]
	v_pk_mul_f32 v[66:67], v[66:67], v[142:143]
	v_pk_mul_f32 v[48:49], v[48:49], v[140:141]
	v_pk_mul_f32 v[50:51], v[50:51], v[142:143]
	v_pk_mul_f32 v[32:33], v[32:33], v[140:141]
	v_pk_mul_f32 v[34:35], v[34:35], v[142:143]
	v_pk_mul_f32 v[16:17], v[16:17], v[140:141]
	v_pk_mul_f32 v[18:19], v[18:19], v[142:143]

.Lm_m35_s2:
	s_sub_i32 s5, s77, 1
	s_cmp_lg_u32 s5, s42
	s_cbranch_scc1 .Lm_m35_end
	ds_read_b128 v[166:169], v207 offset:24576
	ds_read_b128 v[170:173], v208 offset:24576
	ds_read_b128 v[174:177], v207 offset:26624
	ds_read_b128 v[178:181], v208 offset:26624
	ds_read_b128 v[182:185], v207 offset:28672
	ds_read_b128 v[186:189], v208 offset:28672
	s_waitcnt lgkmcnt(4)
	v_mfma_f32_32x32x64_f8f6f4 v[52:67], v[248:255], v[166:173], v[52:67]
	ds_read_b128 v[166:169], v207 offset:30720
	ds_read_b128 v[170:173], v208 offset:30720
	s_waitcnt lgkmcnt(4)
	v_mfma_f32_32x32x64_f8f6f4 v[36:51], v[248:255], v[174:181], v[36:51]
	s_waitcnt lgkmcnt(2)
	v_mfma_f32_32x32x64_f8f6f4 v[20:35], v[248:255], v[182:189], v[20:35]
	s_waitcnt lgkmcnt(0)
	v_mfma_f32_32x32x64_f8f6f4 v[4:19], v[248:255], v[166:173], v[4:19]
	s_nop 7
	v_fma_f32 v2, v2, v217, v124
	v_mov_b32_e32 v217, 1.0
	s_branch .Lm_m35_end
